# speedup vs baseline: 1.0063x; 1.0063x over previous
_Z15prologue_kernel8PrepArgsPKfS1_PKiS1_PDF16_Pf:
	s_mov_b64 s[4:5], -1
	s_cmpk_gt_u32 s2, 0x47f
	v_lshl_or_b32 v2, s2, 8, v0
	v_and_b32_e32 v22, 63, v0
	s_cbranch_scc0 .LBB0_12
	v_add_u32_e32 v4, 0xfffb8000, v2
	v_ashrrev_i32_e32 v1, 6, v4
	v_cmp_gt_u32_e32 vcc, 4, v22
	s_and_saveexec_b64 s[4:5], vcc
	s_cbranch_execz .LBB0_3
	s_load_dwordx2 s[6:7], s[0:1], 0xb0
	v_lshl_or_b32 v6, v1, 2, v22
	v_ashrrev_i32_e32 v7, 31, v6
	v_mov_b32_e32 v3, 0x43ffff58
	v_cmp_eq_u32_e32 vcc, 0, v22
	s_waitcnt lgkmcnt(0)
	v_lshl_add_u64 v[10:11], v[6:7], 4, s[6:7]
	v_mov_b32_e32 v6, 0
	v_cndmask_b32_e32 v7, 0, v3, vcc
	v_mov_b32_e32 v8, v6
	v_mov_b32_e32 v9, v6
	global_store_dwordx4 v[10:11], v[6:9], off sc1

.LBB0_11:
	s_or_b64 exec, exec, s[6:7]
	v_lshlrev_b32_e32 v6, 5, v22
	v_mov_b32_e32 v7, 0
	v_lshl_add_u64 v[14:15], v[10:11], 0, v[6:7]
	global_load_dwordx4 v[6:9], v[14:15], off
	global_load_dwordx4 v[10:13], v[14:15], off offset:16
	v_ashrrev_i32_e32 v5, 31, v4
	s_waitcnt lgkmcnt(0)
	v_lshl_add_u64 v[14:15], v[4:5], 4, s[4:5]
	s_mov_b64 s[4:5], 0
	s_waitcnt vmcnt(1)
	v_cvt_f16_f32_e32 v1, v6
	v_cvt_pk_f16_f32 v3, v7, v8
	s_waitcnt vmcnt(0)
	v_cvt_f16_f32_e32 v8, v13
	v_cvt_pk_f16_f32 v4, v9, v10
	v_cvt_pk_f16_f32 v7, v11, v12
	v_alignbit_b32 v5, v4, v3, 16
	v_alignbit_b32 v6, v7, v4, 16
	v_pack_b32_f16 v4, v1, v3
	v_alignbit_b32 v7, v8, v7, 16
	global_store_dwordx4 v[14:15], v[4:7], off sc1

.LBB0_30:
	s_or_b64 exec, exec, s[0:1]
	s_waitcnt vmcnt(0)
	v_cvt_f16_f32_e32 v25, v0
	v_cvt_f16_f32_e32 v26, v1
	v_cvt_f16_f32_e32 v27, v2
	v_cvt_f16_f32_e32 v28, v3
	v_cvt_f16_f32_e32 v29, v4
	v_cvt_f16_f32_e32 v30, v5
	v_cvt_f16_f32_e32 v31, v6
	v_cvt_f16_f32_e32 v32, v7
	v_cvt_pk_f16_f32 v7, v6, v7
	v_cvt_pk_f16_f32 v6, v4, v5
	v_cvt_pk_f16_f32 v5, v2, v3
	v_cvt_f32_f16_e32 v2, v25
	v_cvt_f32_f16_e32 v3, v26
	v_cvt_f32_f16_e32 v25, v27
	v_cvt_f32_f16_e32 v26, v28
	v_cvt_pk_f16_f32 v4, v0, v1
	v_cvt_f32_f16_e32 v1, v29
	v_add_f32_e32 v0, v2, v3
	v_cvt_f32_f16_e32 v2, v30
	v_add_f32_e32 v0, v0, v25
	v_cvt_f32_f16_e32 v3, v31
	v_add_f32_e32 v0, v0, v26
	v_cvt_f32_f16_e32 v25, v32
	v_add_f32_e32 v0, v0, v1
	v_add_f32_e32 v0, v0, v2
	v_add_f32_e32 v0, v0, v3
	v_add_u32_e32 v24, 0x200, v24
	v_add_f32_e32 v0, v0, v25
	v_cmp_ge_u32_e64 s[0:1], v24, v9
	v_add_f32_e32 v10, v10, v0
	global_store_dwordx4 v[20:21], v[4:7], off sc1
	v_lshl_add_u64 v[20:21], v[20:21], 0, s[4:5]
	v_lshl_add_u64 v[12:13], v[12:13], 0, s[6:7]
	v_lshl_add_u64 v[16:17], v[16:17], 0, s[6:7]
	s_or_b64 s[2:3], s[0:1], s[2:3]
	v_lshl_add_u64 v[14:15], v[14:15], 0, s[6:7]
	s_andn2_b64 exec, exec, s[2:3]
	s_cbranch_execz .LBB0_33

.LBB6_12:
	ds_read_b128 v[176:179], v169
	ds_read_b128 v[180:183], v170
	ds_read_b128 v[184:187], v171
	ds_read_b128 v[188:191], v172
	v_add_u32_e32 v174, 0xc000, v152
	v_lshl_add_u64 v[192:193], v[136:137], 0, s[44:45]
	v_readfirstlane_b32 s47, v174
	v_add_u32_e32 v175, 0xe000, v152
	v_add_u32_e32 v173, s17, v168
	v_lshl_add_u64 v[232:233], v[192:193], 0, s[30:31]
	s_mov_b32 m0, s47
	v_lshl_add_u64 v[248:249], v[134:135], 0, s[44:45]
	v_readfirstlane_b32 s47, v175
	ds_read_b128 v[196:199], v173
	ds_read_b128 v[200:203], v173 offset:1024
	ds_read_b128 v[204:207], v173 offset:2048
	ds_read_b128 v[212:215], v173 offset:3072
	ds_read_b128 v[216:219], v173 offset:4096
	ds_read_b128 v[220:223], v173 offset:5120
	ds_read_b128 v[224:227], v173 offset:6144
	ds_read_b128 v[228:231], v173 offset:7168
	global_load_lds_dwordx4 v[232:233], off
	v_lshl_add_u64 v[232:233], v[248:249], 0, s[30:31]
	s_mov_b32 m0, s47
	s_nop 0
	global_load_lds_dwordx4 v[232:233], off
	s_waitcnt lgkmcnt(8)
	s_barrier
	s_waitcnt lgkmcnt(0)
	v_mfma_f32_16x16x32_f16 v[2:5], v[196:199], v[176:179], v[2:5]
	v_mfma_f32_16x16x32_f16 v[6:9], v[196:199], v[184:187], v[6:9]
	v_mfma_f32_16x16x32_f16 v[10:13], v[204:207], v[176:179], v[10:13]
	v_mfma_f32_16x16x32_f16 v[18:21], v[204:207], v[184:187], v[18:21]
	v_mfma_f32_16x16x32_f16 v[30:33], v[216:219], v[176:179], v[30:33]
	v_mfma_f32_16x16x32_f16 v[42:45], v[216:219], v[184:187], v[42:45]
	v_mfma_f32_16x16x32_f16 v[54:57], v[224:227], v[176:179], v[54:57]
	v_mfma_f32_16x16x32_f16 v[66:69], v[224:227], v[184:187], v[66:69]
	v_mfma_f32_16x16x32_f16 v[2:5], v[200:203], v[180:183], v[2:5]
	v_mfma_f32_16x16x32_f16 v[6:9], v[200:203], v[188:191], v[6:9]
	v_mfma_f32_16x16x32_f16 v[10:13], v[212:215], v[180:183], v[10:13]
	v_mfma_f32_16x16x32_f16 v[18:21], v[212:215], v[188:191], v[18:21]
	v_mfma_f32_16x16x32_f16 v[30:33], v[220:223], v[180:183], v[30:33]
	v_mfma_f32_16x16x32_f16 v[42:45], v[220:223], v[188:191], v[42:45]
	v_mfma_f32_16x16x32_f16 v[54:57], v[228:231], v[180:183], v[54:57]
	v_mfma_f32_16x16x32_f16 v[66:69], v[228:231], v[188:191], v[66:69]
	s_barrier
	v_lshl_add_u64 v[250:251], v[140:141], 0, s[44:45]
	v_readfirstlane_b32 s47, v146
	v_lshl_add_u64 v[252:253], v[250:251], 0, s[34:35]
	s_mov_b32 m0, s47
	ds_read_b128 v[232:235], v161
	ds_read_b128 v[236:239], v162
	ds_read_b128 v[240:243], v163
	ds_read_b128 v[244:247], v164
	global_load_lds_dwordx4 v[252:253], off
	v_lshl_add_u64 v[252:253], v[138:139], 0, s[44:45]
	v_readfirstlane_b32 s47, v147
	v_lshl_add_u64 v[254:255], v[252:253], 0, s[34:35]
	s_mov_b32 m0, s47
	s_nop 0
	global_load_lds_dwordx4 v[254:255], off
	s_barrier
	s_waitcnt lgkmcnt(0)
	v_mfma_f32_16x16x32_f16 v[14:17], v[196:199], v[232:235], v[14:17]
	v_mfma_f32_16x16x32_f16 v[22:25], v[196:199], v[240:243], v[22:25]
	v_mfma_f32_16x16x32_f16 v[34:37], v[204:207], v[232:235], v[34:37]
	v_mfma_f32_16x16x32_f16 v[46:49], v[204:207], v[240:243], v[46:49]
	v_mfma_f32_16x16x32_f16 v[58:61], v[216:219], v[232:235], v[58:61]
	v_mfma_f32_16x16x32_f16 v[70:73], v[216:219], v[240:243], v[70:73]
	v_mfma_f32_16x16x32_f16 v[78:81], v[224:227], v[232:235], v[78:81]
	v_mfma_f32_16x16x32_f16 v[86:89], v[224:227], v[240:243], v[86:89]
	v_mfma_f32_16x16x32_f16 v[14:17], v[200:203], v[236:239], v[14:17]
	v_mfma_f32_16x16x32_f16 v[22:25], v[200:203], v[244:247], v[22:25]
	v_mfma_f32_16x16x32_f16 v[34:37], v[212:215], v[236:239], v[34:37]
	v_mfma_f32_16x16x32_f16 v[46:49], v[212:215], v[244:247], v[46:49]
	v_mfma_f32_16x16x32_f16 v[58:61], v[220:223], v[236:239], v[58:61]
	v_mfma_f32_16x16x32_f16 v[70:73], v[220:223], v[244:247], v[70:73]
	v_mfma_f32_16x16x32_f16 v[78:81], v[228:231], v[236:239], v[78:81]
	v_mfma_f32_16x16x32_f16 v[86:89], v[228:231], v[244:247], v[86:89]
	v_readfirstlane_b32 s47, v152
	v_lshl_add_u64 v[254:255], v[192:193], 0, s[34:35]
	s_mov_b32 m0, s47
	v_readfirstlane_b32 s47, v153
	s_barrier
	ds_read_b128 v[196:199], v173 offset:16384
	ds_read_b128 v[200:203], v173 offset:17408
	ds_read_b128 v[204:207], v173 offset:18432
	ds_read_b128 v[212:215], v173 offset:19456
	ds_read_b128 v[216:219], v173 offset:20480
	ds_read_b128 v[220:223], v173 offset:21504
	ds_read_b128 v[224:227], v173 offset:22528
	ds_read_b128 v[228:231], v173 offset:23552
	global_load_lds_dwordx4 v[254:255], off
	v_lshl_add_u64 v[254:255], v[248:249], 0, s[34:35]
	s_mov_b32 m0, s47
	s_nop 0
	global_load_lds_dwordx4 v[254:255], off
	s_barrier
	s_waitcnt lgkmcnt(0)
	v_mfma_f32_16x16x32_f16 v[26:29], v[196:199], v[176:179], v[26:29]
	v_mfma_f32_16x16x32_f16 v[38:41], v[196:199], v[184:187], v[38:41]
	v_mfma_f32_16x16x32_f16 v[50:53], v[204:207], v[176:179], v[50:53]
	v_mfma_f32_16x16x32_f16 v[62:65], v[204:207], v[184:187], v[62:65]
	v_mfma_f32_16x16x32_f16 v[74:77], v[216:219], v[176:179], v[74:77]
	v_mfma_f32_16x16x32_f16 v[82:85], v[216:219], v[184:187], v[82:85]
	v_mfma_f32_16x16x32_f16 v[90:93], v[224:227], v[176:179], v[90:93]
	v_mfma_f32_16x16x32_f16 v[94:97], v[224:227], v[184:187], v[94:97]
	v_mfma_f32_16x16x32_f16 v[26:29], v[200:203], v[180:183], v[26:29]
	v_mfma_f32_16x16x32_f16 v[38:41], v[200:203], v[188:191], v[38:41]
	v_mfma_f32_16x16x32_f16 v[50:53], v[212:215], v[180:183], v[50:53]
	v_mfma_f32_16x16x32_f16 v[62:65], v[212:215], v[188:191], v[62:65]
	v_mfma_f32_16x16x32_f16 v[74:77], v[220:223], v[180:183], v[74:77]
	v_mfma_f32_16x16x32_f16 v[82:85], v[220:223], v[188:191], v[82:85]
	v_mfma_f32_16x16x32_f16 v[90:93], v[228:231], v[180:183], v[90:93]
	v_mfma_f32_16x16x32_f16 v[94:97], v[228:231], v[188:191], v[94:97]
	s_barrier
	v_readfirstlane_b32 s47, v154
	v_lshl_add_u64 v[176:177], v[250:251], 0, s[36:37]
	s_mov_b32 m0, s47
	v_readfirstlane_b32 s47, v155
	global_load_lds_dwordx4 v[176:177], off
	v_lshl_add_u64 v[176:177], v[252:253], 0, s[36:37]
	s_mov_b32 m0, s47
	s_nop 0
	global_load_lds_dwordx4 v[176:177], off
	s_waitcnt vmcnt(6)
	s_barrier
	v_mfma_f32_16x16x32_f16 v[98:101], v[196:199], v[232:235], v[98:101]
	v_mfma_f32_16x16x32_f16 v[102:105], v[196:199], v[240:243], v[102:105]
	v_mfma_f32_16x16x32_f16 v[106:109], v[204:207], v[232:235], v[106:109]
	v_mfma_f32_16x16x32_f16 v[110:113], v[204:207], v[240:243], v[110:113]
	v_mfma_f32_16x16x32_f16 v[114:117], v[216:219], v[232:235], v[114:117]
	v_mfma_f32_16x16x32_f16 v[118:121], v[216:219], v[240:243], v[118:121]
	v_mfma_f32_16x16x32_f16 v[122:125], v[224:227], v[232:235], v[122:125]
	v_mfma_f32_16x16x32_f16 v[126:129], v[224:227], v[240:243], v[126:129]
	v_mfma_f32_16x16x32_f16 v[98:101], v[200:203], v[236:239], v[98:101]
	v_mfma_f32_16x16x32_f16 v[102:105], v[200:203], v[244:247], v[102:105]
	v_mfma_f32_16x16x32_f16 v[106:109], v[212:215], v[236:239], v[106:109]
	v_mfma_f32_16x16x32_f16 v[110:113], v[212:215], v[244:247], v[110:113]
	v_mfma_f32_16x16x32_f16 v[114:117], v[220:223], v[236:239], v[114:117]
	v_mfma_f32_16x16x32_f16 v[118:121], v[220:223], v[244:247], v[118:121]
	v_mfma_f32_16x16x32_f16 v[122:125], v[228:231], v[236:239], v[122:125]
	v_mfma_f32_16x16x32_f16 v[126:129], v[228:231], v[244:247], v[126:129]
	s_barrier
	ds_read_b128 v[176:179], v148
	ds_read_b128 v[180:183], v149
	ds_read_b128 v[184:187], v150
	ds_read_b128 v[188:191], v151
	v_readfirstlane_b32 s47, v156
	v_lshl_add_u64 v[232:233], v[192:193], 0, s[36:37]
	s_mov_b32 m0, s47
	v_readfirstlane_b32 s47, v157
	ds_read_b128 v[196:199], v173 offset:32768
	ds_read_b128 v[200:203], v173 offset:33792
	ds_read_b128 v[204:207], v173 offset:34816
	ds_read_b128 v[212:215], v173 offset:35840
	ds_read_b128 v[216:219], v173 offset:36864
	ds_read_b128 v[220:223], v173 offset:37888
	ds_read_b128 v[224:227], v173 offset:38912
	ds_read_b128 v[228:231], v173 offset:39936
	global_load_lds_dwordx4 v[232:233], off
	v_lshl_add_u64 v[232:233], v[248:249], 0, s[36:37]
	s_mov_b32 m0, s47
	s_nop 0
	global_load_lds_dwordx4 v[232:233], off
	s_waitcnt lgkmcnt(8)
	s_barrier
	s_waitcnt lgkmcnt(0)
	v_mfma_f32_16x16x32_f16 v[2:5], v[196:199], v[176:179], v[2:5]
	v_mfma_f32_16x16x32_f16 v[6:9], v[196:199], v[184:187], v[6:9]
	v_mfma_f32_16x16x32_f16 v[10:13], v[204:207], v[176:179], v[10:13]
	v_mfma_f32_16x16x32_f16 v[18:21], v[204:207], v[184:187], v[18:21]
	v_mfma_f32_16x16x32_f16 v[30:33], v[216:219], v[176:179], v[30:33]
	v_mfma_f32_16x16x32_f16 v[42:45], v[216:219], v[184:187], v[42:45]
	v_mfma_f32_16x16x32_f16 v[54:57], v[224:227], v[176:179], v[54:57]
	v_mfma_f32_16x16x32_f16 v[66:69], v[224:227], v[184:187], v[66:69]
	v_mfma_f32_16x16x32_f16 v[2:5], v[200:203], v[180:183], v[2:5]
	v_mfma_f32_16x16x32_f16 v[6:9], v[200:203], v[188:191], v[6:9]
	v_mfma_f32_16x16x32_f16 v[10:13], v[212:215], v[180:183], v[10:13]
	v_mfma_f32_16x16x32_f16 v[18:21], v[212:215], v[188:191], v[18:21]
	v_mfma_f32_16x16x32_f16 v[30:33], v[220:223], v[180:183], v[30:33]
	v_mfma_f32_16x16x32_f16 v[42:45], v[220:223], v[188:191], v[42:45]
	v_mfma_f32_16x16x32_f16 v[54:57], v[228:231], v[180:183], v[54:57]
	v_mfma_f32_16x16x32_f16 v[66:69], v[228:231], v[188:191], v[66:69]
	s_barrier
	v_readfirstlane_b32 s47, v158
	v_lshl_add_u64 v[254:255], v[250:251], 0, s[38:39]
	s_mov_b32 m0, s47
	v_readfirstlane_b32 s47, v159
	ds_read_b128 v[232:235], v142
	ds_read_b128 v[236:239], v143
	ds_read_b128 v[240:243], v144
	ds_read_b128 v[244:247], v145
	global_load_lds_dwordx4 v[254:255], off
	v_lshl_add_u64 v[254:255], v[252:253], 0, s[38:39]
	s_mov_b32 m0, s47
	s_nop 0
	global_load_lds_dwordx4 v[254:255], off
	s_barrier
	s_waitcnt lgkmcnt(0)
	v_mfma_f32_16x16x32_f16 v[14:17], v[196:199], v[232:235], v[14:17]
	v_mfma_f32_16x16x32_f16 v[22:25], v[196:199], v[240:243], v[22:25]
	v_mfma_f32_16x16x32_f16 v[34:37], v[204:207], v[232:235], v[34:37]
	v_mfma_f32_16x16x32_f16 v[46:49], v[204:207], v[240:243], v[46:49]
	v_mfma_f32_16x16x32_f16 v[58:61], v[216:219], v[232:235], v[58:61]
	v_mfma_f32_16x16x32_f16 v[70:73], v[216:219], v[240:243], v[70:73]
	v_mfma_f32_16x16x32_f16 v[78:81], v[224:227], v[232:235], v[78:81]
	v_mfma_f32_16x16x32_f16 v[86:89], v[224:227], v[240:243], v[86:89]
	v_mfma_f32_16x16x32_f16 v[14:17], v[200:203], v[236:239], v[14:17]
	v_mfma_f32_16x16x32_f16 v[22:25], v[200:203], v[244:247], v[22:25]
	v_mfma_f32_16x16x32_f16 v[34:37], v[212:215], v[236:239], v[34:37]
	v_mfma_f32_16x16x32_f16 v[46:49], v[212:215], v[244:247], v[46:49]
	v_mfma_f32_16x16x32_f16 v[58:61], v[220:223], v[236:239], v[58:61]
	v_mfma_f32_16x16x32_f16 v[70:73], v[220:223], v[244:247], v[70:73]
	v_mfma_f32_16x16x32_f16 v[78:81], v[228:231], v[236:239], v[78:81]
	v_mfma_f32_16x16x32_f16 v[86:89], v[228:231], v[244:247], v[86:89]
	v_readfirstlane_b32 s47, v160
	v_lshl_add_u64 v[192:193], v[192:193], 0, s[38:39]
	s_mov_b32 m0, s47
	v_readfirstlane_b32 s47, v165
	s_barrier
	ds_read_b128 v[196:199], v173 offset:49152
	ds_read_b128 v[200:203], v173 offset:50176
	ds_read_b128 v[204:207], v173 offset:51200
	ds_read_b128 v[212:215], v173 offset:52224
	ds_read_b128 v[216:219], v173 offset:53248
	ds_read_b128 v[220:223], v173 offset:54272
	ds_read_b128 v[224:227], v173 offset:55296
	ds_read_b128 v[228:231], v173 offset:56320
	global_load_lds_dwordx4 v[192:193], off
	v_lshl_add_u64 v[192:193], v[248:249], 0, s[38:39]
	s_mov_b32 m0, s47
	s_nop 0
	global_load_lds_dwordx4 v[192:193], off
	s_barrier
	s_waitcnt lgkmcnt(0)
	v_mfma_f32_16x16x32_f16 v[26:29], v[196:199], v[176:179], v[26:29]
	v_mfma_f32_16x16x32_f16 v[38:41], v[196:199], v[184:187], v[38:41]
	v_mfma_f32_16x16x32_f16 v[50:53], v[204:207], v[176:179], v[50:53]
	v_mfma_f32_16x16x32_f16 v[62:65], v[204:207], v[184:187], v[62:65]
	v_mfma_f32_16x16x32_f16 v[74:77], v[216:219], v[176:179], v[74:77]
	v_mfma_f32_16x16x32_f16 v[82:85], v[216:219], v[184:187], v[82:85]
	v_mfma_f32_16x16x32_f16 v[90:93], v[224:227], v[176:179], v[90:93]
	v_mfma_f32_16x16x32_f16 v[94:97], v[224:227], v[184:187], v[94:97]
	v_mfma_f32_16x16x32_f16 v[26:29], v[200:203], v[180:183], v[26:29]
	v_mfma_f32_16x16x32_f16 v[38:41], v[200:203], v[188:191], v[38:41]
	v_mfma_f32_16x16x32_f16 v[50:53], v[212:215], v[180:183], v[50:53]
	v_mfma_f32_16x16x32_f16 v[62:65], v[212:215], v[188:191], v[62:65]
	v_mfma_f32_16x16x32_f16 v[74:77], v[220:223], v[180:183], v[74:77]
	v_mfma_f32_16x16x32_f16 v[82:85], v[220:223], v[188:191], v[82:85]
	v_mfma_f32_16x16x32_f16 v[90:93], v[228:231], v[180:183], v[90:93]
	v_mfma_f32_16x16x32_f16 v[94:97], v[228:231], v[188:191], v[94:97]
	s_barrier
	v_readfirstlane_b32 s47, v166
	v_lshl_add_u64 v[176:177], v[250:251], 0, s[40:41]
	s_mov_b32 m0, s47
	v_readfirstlane_b32 s47, v167
	global_load_lds_dwordx4 v[176:177], off
	v_lshl_add_u64 v[176:177], v[252:253], 0, s[40:41]
	s_mov_b32 m0, s47
	s_nop 0
	global_load_lds_dwordx4 v[176:177], off
	s_waitcnt vmcnt(6)
	s_barrier
	v_mfma_f32_16x16x32_f16 v[98:101], v[196:199], v[232:235], v[98:101]
	v_mfma_f32_16x16x32_f16 v[102:105], v[196:199], v[240:243], v[102:105]
	v_mfma_f32_16x16x32_f16 v[106:109], v[204:207], v[232:235], v[106:109]
	v_mfma_f32_16x16x32_f16 v[110:113], v[204:207], v[240:243], v[110:113]
	v_mfma_f32_16x16x32_f16 v[114:117], v[216:219], v[232:235], v[114:117]
	v_mfma_f32_16x16x32_f16 v[118:121], v[216:219], v[240:243], v[118:121]
	v_mfma_f32_16x16x32_f16 v[122:125], v[224:227], v[232:235], v[122:125]
	v_mfma_f32_16x16x32_f16 v[126:129], v[224:227], v[240:243], v[126:129]
	v_mfma_f32_16x16x32_f16 v[98:101], v[200:203], v[236:239], v[98:101]
	v_mfma_f32_16x16x32_f16 v[102:105], v[200:203], v[244:247], v[102:105]
	v_mfma_f32_16x16x32_f16 v[106:109], v[212:215], v[236:239], v[106:109]
	v_mfma_f32_16x16x32_f16 v[110:113], v[212:215], v[244:247], v[110:113]
	v_mfma_f32_16x16x32_f16 v[114:117], v[220:223], v[236:239], v[114:117]
	v_mfma_f32_16x16x32_f16 v[118:121], v[220:223], v[244:247], v[118:121]
	v_mfma_f32_16x16x32_f16 v[122:125], v[228:231], v[236:239], v[122:125]
	v_mfma_f32_16x16x32_f16 v[126:129], v[228:231], v[244:247], v[126:129]
	s_add_i32 s46, s46, 2
	s_add_u32 s44, s44, 0x100
	s_addc_u32 s45, s45, 0
	s_cmp_lt_u32 s46, 4
	s_barrier
	s_cbranch_scc1 .LBB6_12
	s_add_u32 s0, s0, 0x20380
	s_addc_u32 s1, s1, 0
	v_readfirstlane_b32 s17, v174
	v_lshl_add_u64 v[130:131], v[130:131], 1, s[0:1]
	s_mov_b32 m0, s17
	ds_read_b128 v[134:137], v169
	ds_read_b128 v[138:141], v170
	ds_read_b128 v[152:155], v171
	ds_read_b128 v[156:159], v172
	ds_read_b128 v[166:169], v173
	ds_read_b128 v[176:179], v173 offset:1024
	ds_read_b128 v[180:183], v173 offset:2048
	ds_read_b128 v[184:187], v173 offset:3072
	ds_read_b128 v[188:191], v173 offset:4096
	ds_read_b128 v[196:199], v173 offset:5120
	ds_read_b128 v[200:203], v173 offset:6144
	ds_read_b128 v[204:207], v173 offset:7168
	global_load_lds_dwordx4 v[130:131], off
	v_lshl_add_u64 v[130:131], v[132:133], 1, s[0:1]
	v_readfirstlane_b32 s0, v175
	s_mov_b32 m0, s0
	s_nop 0
	global_load_lds_dwordx4 v[130:131], off
	s_barrier
	s_waitcnt lgkmcnt(0)
	v_mfma_f32_16x16x32_f16 v[2:5], v[166:169], v[134:137], v[2:5]
	v_mfma_f32_16x16x32_f16 v[42:45], v[188:191], v[152:155], v[42:45]
	v_mfma_f32_16x16x32_f16 v[54:57], v[200:203], v[134:137], v[54:57]
	v_mfma_f32_16x16x32_f16 v[66:69], v[200:203], v[152:155], v[66:69]
	v_mfma_f32_16x16x32_f16 v[2:5], v[176:179], v[138:141], v[2:5]
	v_mfma_f32_16x16x32_f16 v[6:9], v[166:169], v[152:155], v[6:9]
	v_mfma_f32_16x16x32_f16 v[10:13], v[180:183], v[134:137], v[10:13]
	v_mfma_f32_16x16x32_f16 v[18:21], v[180:183], v[152:155], v[18:21]
	v_mfma_f32_16x16x32_f16 v[30:33], v[188:191], v[134:137], v[30:33]
	v_mfma_f32_16x16x32_f16 v[42:45], v[196:199], v[156:159], v[42:45]
	v_mfma_f32_16x16x32_f16 v[54:57], v[204:207], v[138:141], v[54:57]
	v_mfma_f32_16x16x32_f16 v[66:69], v[204:207], v[156:159], v[66:69]
	v_mfma_f32_16x16x32_f16 v[6:9], v[176:179], v[156:159], v[6:9]
	v_mfma_f32_16x16x32_f16 v[10:13], v[184:187], v[138:141], v[10:13]
	v_mfma_f32_16x16x32_f16 v[18:21], v[184:187], v[156:159], v[18:21]
	v_mfma_f32_16x16x32_f16 v[30:33], v[196:199], v[138:141], v[30:33]
	s_barrier
	ds_read_b128 v[130:133], v161
	ds_read_b128 v[212:215], v162
	ds_read_b128 v[160:163], v163
	ds_read_b128 v[216:219], v164
	s_barrier
	s_waitcnt lgkmcnt(0)
	v_mfma_f32_16x16x32_f16 v[14:17], v[166:169], v[130:133], v[14:17]
	v_mfma_f32_16x16x32_f16 v[78:81], v[200:203], v[130:133], v[78:81]
	v_mfma_f32_16x16x32_f16 v[14:17], v[176:179], v[212:215], v[14:17]
	v_mfma_f32_16x16x32_f16 v[22:25], v[166:169], v[160:163], v[22:25]
	v_mfma_f32_16x16x32_f16 v[34:37], v[180:183], v[130:133], v[34:37]
	v_mfma_f32_16x16x32_f16 v[46:49], v[180:183], v[160:163], v[46:49]
	v_mfma_f32_16x16x32_f16 v[58:61], v[188:191], v[130:133], v[58:61]
	v_mfma_f32_16x16x32_f16 v[70:73], v[188:191], v[160:163], v[70:73]
	v_mfma_f32_16x16x32_f16 v[164:167], v[204:207], v[212:215], v[78:81]
	v_mfma_f32_16x16x32_f16 v[78:81], v[200:203], v[160:163], v[86:89]
	v_mfma_f32_16x16x32_f16 v[22:25], v[176:179], v[216:219], v[22:25]
	v_mfma_f32_16x16x32_f16 v[34:37], v[184:187], v[212:215], v[34:37]
	v_mfma_f32_16x16x32_f16 v[46:49], v[184:187], v[216:219], v[46:49]
	v_mfma_f32_16x16x32_f16 v[58:61], v[196:199], v[212:215], v[58:61]
	v_mfma_f32_16x16x32_f16 v[70:73], v[196:199], v[216:219], v[70:73]
	v_mfma_f32_16x16x32_f16 v[86:89], v[204:207], v[216:219], v[78:81]
	s_barrier
	s_nop 0
	ds_read_b128 v[78:81], v173 offset:16384
	ds_read_b128 v[168:171], v173 offset:17408
	ds_read_b128 v[174:177], v173 offset:18432
	ds_read_b128 v[178:181], v173 offset:19456
	ds_read_b128 v[182:185], v173 offset:20480
	ds_read_b128 v[186:189], v173 offset:21504
	ds_read_b128 v[190:193], v173 offset:22528
	ds_read_b128 v[196:199], v173 offset:23552
	s_waitcnt vmcnt(4)
	s_barrier
	s_waitcnt lgkmcnt(0)
	v_mfma_f32_16x16x32_f16 v[26:29], v[78:81], v[134:137], v[26:29]
	v_mfma_f32_16x16x32_f16 v[38:41], v[78:81], v[152:155], v[38:41]
	v_mfma_f32_16x16x32_f16 v[26:29], v[168:171], v[138:141], v[26:29]
	v_mfma_f32_16x16x32_f16 v[38:41], v[168:171], v[156:159], v[38:41]
	v_mfma_f32_16x16x32_f16 v[50:53], v[174:177], v[134:137], v[50:53]
	v_mfma_f32_16x16x32_f16 v[62:65], v[174:177], v[152:155], v[62:65]
	v_mfma_f32_16x16x32_f16 v[74:77], v[182:185], v[134:137], v[74:77]
	v_mfma_f32_16x16x32_f16 v[82:85], v[182:185], v[152:155], v[82:85]
	v_mfma_f32_16x16x32_f16 v[90:93], v[190:193], v[134:137], v[90:93]
	v_mfma_f32_16x16x32_f16 v[94:97], v[190:193], v[152:155], v[94:97]
	v_mfma_f32_16x16x32_f16 v[50:53], v[178:181], v[138:141], v[50:53]
	v_mfma_f32_16x16x32_f16 v[62:65], v[178:181], v[156:159], v[62:65]
	v_mfma_f32_16x16x32_f16 v[74:77], v[186:189], v[138:141], v[74:77]
	v_mfma_f32_16x16x32_f16 v[82:85], v[186:189], v[156:159], v[82:85]
	v_mfma_f32_16x16x32_f16 v[90:93], v[196:199], v[138:141], v[90:93]
	v_mfma_f32_16x16x32_f16 v[94:97], v[196:199], v[156:159], v[94:97]
	v_mfma_f32_16x16x32_f16 v[98:101], v[78:81], v[130:133], v[98:101]
	v_mfma_f32_16x16x32_f16 v[78:81], v[78:81], v[160:163], v[102:105]
	v_mfma_f32_16x16x32_f16 v[102:105], v[168:171], v[216:219], v[78:81]
	v_mfma_f32_16x16x32_f16 v[78:81], v[174:177], v[130:133], v[106:109]
	v_mfma_f32_16x16x32_f16 v[106:109], v[178:181], v[212:215], v[78:81]
	v_mfma_f32_16x16x32_f16 v[78:81], v[174:177], v[160:163], v[110:113]
	v_mfma_f32_16x16x32_f16 v[200:203], v[178:181], v[216:219], v[78:81]
	v_mfma_f32_16x16x32_f16 v[78:81], v[182:185], v[130:133], v[114:117]
	v_mfma_f32_16x16x32_f16 v[204:207], v[186:189], v[212:215], v[78:81]
	v_mfma_f32_16x16x32_f16 v[78:81], v[182:185], v[160:163], v[118:121]
	v_mfma_f32_16x16x32_f16 v[220:223], v[186:189], v[216:219], v[78:81]
	v_mfma_f32_16x16x32_f16 v[78:81], v[190:193], v[130:133], v[122:125]
	v_mfma_f32_16x16x32_f16 v[98:101], v[168:171], v[212:215], v[98:101]
	v_mfma_f32_16x16x32_f16 v[212:215], v[196:199], v[212:215], v[78:81]
	v_mfma_f32_16x16x32_f16 v[78:81], v[190:193], v[160:163], v[126:129]
	v_mfma_f32_16x16x32_f16 v[196:199], v[196:199], v[216:219], v[78:81]
	s_barrier
	ds_read_b128 v[110:113], v148
	ds_read_b128 v[130:133], v149
	ds_read_b128 v[216:219], v150
	ds_read_b128 v[224:227], v151
	s_nop 0
	ds_read_b128 v[78:81], v173 offset:32768
	ds_read_b128 v[114:117], v173 offset:33792
	ds_read_b128 v[118:121], v173 offset:34816
	ds_read_b128 v[134:137], v173 offset:35840
	ds_read_b128 v[138:141], v173 offset:36864
	ds_read_b128 v[168:171], v173 offset:37888
	ds_read_b128 v[174:177], v173 offset:38912
	ds_read_b128 v[228:231], v173 offset:39936
	s_waitcnt vmcnt(2)
	s_barrier
	s_waitcnt lgkmcnt(0)
	v_mfma_f32_16x16x32_f16 v[2:5], v[78:81], v[110:113], v[2:5]
	v_mfma_f32_16x16x32_f16 v[190:193], v[114:117], v[130:133], v[2:5]
	v_mfma_f32_16x16x32_f16 v[2:5], v[78:81], v[216:219], v[6:9]
	v_mfma_f32_16x16x32_f16 v[158:161], v[114:117], v[224:227], v[2:5]
	v_mfma_f32_16x16x32_f16 v[2:5], v[118:121], v[110:113], v[10:13]
	v_mfma_f32_16x16x32_f16 v[186:189], v[134:137], v[130:133], v[2:5]
	v_mfma_f32_16x16x32_f16 v[2:5], v[118:121], v[216:219], v[18:21]
	v_mfma_f32_16x16x32_f16 v[154:157], v[134:137], v[224:227], v[2:5]
	v_mfma_f32_16x16x32_f16 v[2:5], v[138:141], v[110:113], v[30:33]
	v_mfma_f32_16x16x32_f16 v[182:185], v[168:171], v[130:133], v[2:5]
	v_mfma_f32_16x16x32_f16 v[2:5], v[138:141], v[216:219], v[42:45]
	v_mfma_f32_16x16x32_f16 v[150:153], v[168:171], v[224:227], v[2:5]
	v_mfma_f32_16x16x32_f16 v[2:5], v[174:177], v[110:113], v[54:57]
	v_mfma_f32_16x16x32_f16 v[178:181], v[228:231], v[130:133], v[2:5]
	v_mfma_f32_16x16x32_f16 v[2:5], v[174:177], v[216:219], v[66:69]
	v_mfma_f32_16x16x32_f16 v[146:149], v[228:231], v[224:227], v[2:5]
	s_barrier
	s_nop 4
	ds_read_b128 v[2:5], v142
	ds_read_b128 v[6:9], v143
	ds_read_b128 v[10:13], v144
	ds_read_b128 v[18:21], v145
	s_waitcnt vmcnt(0)
	s_barrier
	s_waitcnt lgkmcnt(0)
	v_mfma_f32_16x16x32_f16 v[14:17], v[78:81], v[2:5], v[14:17]
	v_mfma_f32_16x16x32_f16 v[126:129], v[114:117], v[6:9], v[14:17]
	v_mfma_f32_16x16x32_f16 v[14:17], v[78:81], v[10:13], v[22:25]
	v_mfma_f32_16x16x32_f16 v[78:81], v[114:117], v[18:21], v[14:17]
	v_mfma_f32_16x16x32_f16 v[14:17], v[118:121], v[2:5], v[34:37]
	v_mfma_f32_16x16x32_f16 v[122:125], v[134:137], v[6:9], v[14:17]
	v_mfma_f32_16x16x32_f16 v[14:17], v[118:121], v[10:13], v[46:49]
	v_mfma_f32_16x16x32_f16 v[66:69], v[134:137], v[18:21], v[14:17]
	v_mfma_f32_16x16x32_f16 v[14:17], v[138:141], v[2:5], v[58:61]
	v_mfma_f32_16x16x32_f16 v[118:121], v[168:171], v[6:9], v[14:17]
	v_mfma_f32_16x16x32_f16 v[14:17], v[138:141], v[10:13], v[70:73]
	v_mfma_f32_16x16x32_f16 v[54:57], v[168:171], v[18:21], v[14:17]
	v_mfma_f32_16x16x32_f16 v[14:17], v[174:177], v[2:5], v[164:167]
	v_mfma_f32_16x16x32_f16 v[114:117], v[228:231], v[6:9], v[14:17]
	v_mfma_f32_16x16x32_f16 v[14:17], v[174:177], v[10:13], v[86:89]
	v_mfma_f32_16x16x32_f16 v[42:45], v[228:231], v[18:21], v[14:17]
	s_barrier
	s_nop 4
	ds_read_b128 v[14:17], v173 offset:49152
	ds_read_b128 v[22:25], v173 offset:50176
	ds_read_b128 v[30:33], v173 offset:51200
	ds_read_b128 v[34:37], v173 offset:52224
	ds_read_b128 v[46:49], v173 offset:53248
	ds_read_b128 v[58:61], v173 offset:54272
	ds_read_b128 v[70:73], v173 offset:55296
	ds_read_b128 v[86:89], v173 offset:56320
	s_barrier
	s_waitcnt lgkmcnt(0)
	v_mfma_f32_16x16x32_f16 v[26:29], v[14:17], v[110:113], v[26:29]
	v_mfma_f32_16x16x32_f16 v[174:177], v[22:25], v[130:133], v[26:29]
	v_mfma_f32_16x16x32_f16 v[26:29], v[14:17], v[216:219], v[38:41]
	v_mfma_f32_16x16x32_f16 v[142:145], v[22:25], v[224:227], v[26:29]
	v_mfma_f32_16x16x32_f16 v[26:29], v[30:33], v[110:113], v[50:53]
	v_mfma_f32_16x16x32_f16 v[170:173], v[34:37], v[130:133], v[26:29]
	v_mfma_f32_16x16x32_f16 v[26:29], v[30:33], v[216:219], v[62:65]
	v_mfma_f32_16x16x32_f16 v[138:141], v[34:37], v[224:227], v[26:29]
	v_mfma_f32_16x16x32_f16 v[26:29], v[46:49], v[110:113], v[74:77]
	v_mfma_f32_16x16x32_f16 v[166:169], v[58:61], v[130:133], v[26:29]
	v_mfma_f32_16x16x32_f16 v[26:29], v[46:49], v[216:219], v[82:85]
	v_mfma_f32_16x16x32_f16 v[134:137], v[58:61], v[224:227], v[26:29]
	v_mfma_f32_16x16x32_f16 v[26:29], v[70:73], v[110:113], v[90:93]
	v_mfma_f32_16x16x32_f16 v[162:165], v[86:89], v[130:133], v[26:29]
	v_mfma_f32_16x16x32_f16 v[26:29], v[70:73], v[216:219], v[94:97]
	v_mfma_f32_16x16x32_f16 v[130:133], v[86:89], v[224:227], v[26:29]
	v_mfma_f32_16x16x32_f16 v[26:29], v[14:17], v[2:5], v[98:101]
	v_mfma_f32_16x16x32_f16 v[14:17], v[14:17], v[10:13], v[102:105]
	v_mfma_f32_16x16x32_f16 v[38:41], v[22:25], v[18:21], v[14:17]
	v_mfma_f32_16x16x32_f16 v[14:17], v[30:33], v[2:5], v[106:109]
	v_mfma_f32_16x16x32_f16 v[106:109], v[34:37], v[6:9], v[14:17]
	v_mfma_f32_16x16x32_f16 v[14:17], v[30:33], v[10:13], v[200:203]
	v_mfma_f32_16x16x32_f16 v[110:113], v[22:25], v[6:9], v[26:29]
	v_mfma_f32_16x16x32_f16 v[26:29], v[34:37], v[18:21], v[14:17]
	v_mfma_f32_16x16x32_f16 v[14:17], v[46:49], v[2:5], v[204:207]
	v_mfma_f32_16x16x32_f16 v[2:5], v[70:73], v[2:5], v[212:215]
	v_mfma_f32_16x16x32_f16 v[102:105], v[58:61], v[6:9], v[14:17]
	v_mfma_f32_16x16x32_f16 v[14:17], v[46:49], v[10:13], v[220:223]
	v_mfma_f32_16x16x32_f16 v[98:101], v[86:89], v[6:9], v[2:5]
	v_mfma_f32_16x16x32_f16 v[2:5], v[70:73], v[10:13], v[196:199]
	v_mfma_f32_16x16x32_f16 v[14:17], v[58:61], v[18:21], v[14:17]
	v_mfma_f32_16x16x32_f16 v[2:5], v[86:89], v[18:21], v[2:5]
	s_cmpk_gt_u32 s65, 0xff
	s_barrier
	s_cbranch_scc1 .LBB6_15
	s_barrier

.LBB7_239:
	ds_read_b128 v[176:179], v169
	ds_read_b128 v[180:183], v170
	ds_read_b128 v[184:187], v171
	ds_read_b128 v[188:191], v172
	v_add_u32_e32 v174, 0xc000, v152
	v_lshl_add_u64 v[192:193], v[136:137], 0, s[46:47]
	v_readfirstlane_b32 s49, v174
	v_add_u32_e32 v175, 0xe000, v152
	v_add_u32_e32 v173, s5, v168
	v_lshl_add_u64 v[232:233], v[192:193], 0, s[34:35]
	s_mov_b32 m0, s49
	v_lshl_add_u64 v[248:249], v[134:135], 0, s[46:47]
	v_readfirstlane_b32 s49, v175
	ds_read_b128 v[196:199], v173
	ds_read_b128 v[200:203], v173 offset:1024
	ds_read_b128 v[204:207], v173 offset:2048
	ds_read_b128 v[212:215], v173 offset:3072
	ds_read_b128 v[216:219], v173 offset:4096
	ds_read_b128 v[220:223], v173 offset:5120
	ds_read_b128 v[224:227], v173 offset:6144
	ds_read_b128 v[228:231], v173 offset:7168
	global_load_lds_dwordx4 v[232:233], off
	v_lshl_add_u64 v[232:233], v[248:249], 0, s[34:35]
	s_mov_b32 m0, s49
	s_nop 0
	global_load_lds_dwordx4 v[232:233], off
	s_waitcnt lgkmcnt(8)
	s_barrier
	s_waitcnt lgkmcnt(0)
	v_mfma_f32_16x16x32_f16 v[2:5], v[196:199], v[176:179], v[2:5]
	v_mfma_f32_16x16x32_f16 v[6:9], v[196:199], v[184:187], v[6:9]
	v_mfma_f32_16x16x32_f16 v[10:13], v[204:207], v[176:179], v[10:13]
	v_mfma_f32_16x16x32_f16 v[18:21], v[204:207], v[184:187], v[18:21]
	v_mfma_f32_16x16x32_f16 v[30:33], v[216:219], v[176:179], v[30:33]
	v_mfma_f32_16x16x32_f16 v[42:45], v[216:219], v[184:187], v[42:45]
	v_mfma_f32_16x16x32_f16 v[54:57], v[224:227], v[176:179], v[54:57]
	v_mfma_f32_16x16x32_f16 v[66:69], v[224:227], v[184:187], v[66:69]
	v_mfma_f32_16x16x32_f16 v[2:5], v[200:203], v[180:183], v[2:5]
	v_mfma_f32_16x16x32_f16 v[6:9], v[200:203], v[188:191], v[6:9]
	v_mfma_f32_16x16x32_f16 v[10:13], v[212:215], v[180:183], v[10:13]
	v_mfma_f32_16x16x32_f16 v[18:21], v[212:215], v[188:191], v[18:21]
	v_mfma_f32_16x16x32_f16 v[30:33], v[220:223], v[180:183], v[30:33]
	v_mfma_f32_16x16x32_f16 v[42:45], v[220:223], v[188:191], v[42:45]
	v_mfma_f32_16x16x32_f16 v[54:57], v[228:231], v[180:183], v[54:57]
	v_mfma_f32_16x16x32_f16 v[66:69], v[228:231], v[188:191], v[66:69]
	s_barrier
	v_lshl_add_u64 v[250:251], v[140:141], 0, s[46:47]
	v_readfirstlane_b32 s49, v146
	v_lshl_add_u64 v[252:253], v[250:251], 0, s[36:37]
	s_mov_b32 m0, s49
	ds_read_b128 v[232:235], v161
	ds_read_b128 v[236:239], v162
	ds_read_b128 v[240:243], v163
	ds_read_b128 v[244:247], v164
	global_load_lds_dwordx4 v[252:253], off
	v_lshl_add_u64 v[252:253], v[138:139], 0, s[46:47]
	v_readfirstlane_b32 s49, v147
	v_lshl_add_u64 v[254:255], v[252:253], 0, s[36:37]
	s_mov_b32 m0, s49
	s_nop 0
	global_load_lds_dwordx4 v[254:255], off
	s_barrier
	s_waitcnt lgkmcnt(0)
	v_mfma_f32_16x16x32_f16 v[14:17], v[196:199], v[232:235], v[14:17]
	v_mfma_f32_16x16x32_f16 v[22:25], v[196:199], v[240:243], v[22:25]
	v_mfma_f32_16x16x32_f16 v[34:37], v[204:207], v[232:235], v[34:37]
	v_mfma_f32_16x16x32_f16 v[46:49], v[204:207], v[240:243], v[46:49]
	v_mfma_f32_16x16x32_f16 v[58:61], v[216:219], v[232:235], v[58:61]
	v_mfma_f32_16x16x32_f16 v[70:73], v[216:219], v[240:243], v[70:73]
	v_mfma_f32_16x16x32_f16 v[78:81], v[224:227], v[232:235], v[78:81]
	v_mfma_f32_16x16x32_f16 v[86:89], v[224:227], v[240:243], v[86:89]
	v_mfma_f32_16x16x32_f16 v[14:17], v[200:203], v[236:239], v[14:17]
	v_mfma_f32_16x16x32_f16 v[22:25], v[200:203], v[244:247], v[22:25]
	v_mfma_f32_16x16x32_f16 v[34:37], v[212:215], v[236:239], v[34:37]
	v_mfma_f32_16x16x32_f16 v[46:49], v[212:215], v[244:247], v[46:49]
	v_mfma_f32_16x16x32_f16 v[58:61], v[220:223], v[236:239], v[58:61]
	v_mfma_f32_16x16x32_f16 v[70:73], v[220:223], v[244:247], v[70:73]
	v_mfma_f32_16x16x32_f16 v[78:81], v[228:231], v[236:239], v[78:81]
	v_mfma_f32_16x16x32_f16 v[86:89], v[228:231], v[244:247], v[86:89]
	v_readfirstlane_b32 s49, v152
	v_lshl_add_u64 v[254:255], v[192:193], 0, s[36:37]
	s_mov_b32 m0, s49
	v_readfirstlane_b32 s49, v153
	s_barrier
	ds_read_b128 v[196:199], v173 offset:16384
	ds_read_b128 v[200:203], v173 offset:17408
	ds_read_b128 v[204:207], v173 offset:18432
	ds_read_b128 v[212:215], v173 offset:19456
	ds_read_b128 v[216:219], v173 offset:20480
	ds_read_b128 v[220:223], v173 offset:21504
	ds_read_b128 v[224:227], v173 offset:22528
	ds_read_b128 v[228:231], v173 offset:23552
	global_load_lds_dwordx4 v[254:255], off
	v_lshl_add_u64 v[254:255], v[248:249], 0, s[36:37]
	s_mov_b32 m0, s49
	s_nop 0
	global_load_lds_dwordx4 v[254:255], off
	s_barrier
	s_waitcnt lgkmcnt(0)
	v_mfma_f32_16x16x32_f16 v[26:29], v[196:199], v[176:179], v[26:29]
	v_mfma_f32_16x16x32_f16 v[38:41], v[196:199], v[184:187], v[38:41]
	v_mfma_f32_16x16x32_f16 v[50:53], v[204:207], v[176:179], v[50:53]
	v_mfma_f32_16x16x32_f16 v[62:65], v[204:207], v[184:187], v[62:65]
	v_mfma_f32_16x16x32_f16 v[74:77], v[216:219], v[176:179], v[74:77]
	v_mfma_f32_16x16x32_f16 v[82:85], v[216:219], v[184:187], v[82:85]
	v_mfma_f32_16x16x32_f16 v[90:93], v[224:227], v[176:179], v[90:93]
	v_mfma_f32_16x16x32_f16 v[94:97], v[224:227], v[184:187], v[94:97]
	v_mfma_f32_16x16x32_f16 v[26:29], v[200:203], v[180:183], v[26:29]
	v_mfma_f32_16x16x32_f16 v[38:41], v[200:203], v[188:191], v[38:41]
	v_mfma_f32_16x16x32_f16 v[50:53], v[212:215], v[180:183], v[50:53]
	v_mfma_f32_16x16x32_f16 v[62:65], v[212:215], v[188:191], v[62:65]
	v_mfma_f32_16x16x32_f16 v[74:77], v[220:223], v[180:183], v[74:77]
	v_mfma_f32_16x16x32_f16 v[82:85], v[220:223], v[188:191], v[82:85]
	v_mfma_f32_16x16x32_f16 v[90:93], v[228:231], v[180:183], v[90:93]
	v_mfma_f32_16x16x32_f16 v[94:97], v[228:231], v[188:191], v[94:97]
	s_barrier
	v_readfirstlane_b32 s49, v154
	v_lshl_add_u64 v[176:177], v[250:251], 0, s[38:39]
	s_mov_b32 m0, s49
	v_readfirstlane_b32 s49, v155
	global_load_lds_dwordx4 v[176:177], off
	v_lshl_add_u64 v[176:177], v[252:253], 0, s[38:39]
	s_mov_b32 m0, s49
	s_nop 0
	global_load_lds_dwordx4 v[176:177], off
	s_waitcnt vmcnt(6)
	s_barrier
	v_mfma_f32_16x16x32_f16 v[98:101], v[196:199], v[232:235], v[98:101]
	v_mfma_f32_16x16x32_f16 v[102:105], v[196:199], v[240:243], v[102:105]
	v_mfma_f32_16x16x32_f16 v[106:109], v[204:207], v[232:235], v[106:109]
	v_mfma_f32_16x16x32_f16 v[110:113], v[204:207], v[240:243], v[110:113]
	v_mfma_f32_16x16x32_f16 v[114:117], v[216:219], v[232:235], v[114:117]
	v_mfma_f32_16x16x32_f16 v[118:121], v[216:219], v[240:243], v[118:121]
	v_mfma_f32_16x16x32_f16 v[122:125], v[224:227], v[232:235], v[122:125]
	v_mfma_f32_16x16x32_f16 v[126:129], v[224:227], v[240:243], v[126:129]
	v_mfma_f32_16x16x32_f16 v[98:101], v[200:203], v[236:239], v[98:101]
	v_mfma_f32_16x16x32_f16 v[102:105], v[200:203], v[244:247], v[102:105]
	v_mfma_f32_16x16x32_f16 v[106:109], v[212:215], v[236:239], v[106:109]
	v_mfma_f32_16x16x32_f16 v[110:113], v[212:215], v[244:247], v[110:113]
	v_mfma_f32_16x16x32_f16 v[114:117], v[220:223], v[236:239], v[114:117]
	v_mfma_f32_16x16x32_f16 v[118:121], v[220:223], v[244:247], v[118:121]
	v_mfma_f32_16x16x32_f16 v[122:125], v[228:231], v[236:239], v[122:125]
	v_mfma_f32_16x16x32_f16 v[126:129], v[228:231], v[244:247], v[126:129]
	s_barrier
	ds_read_b128 v[176:179], v148
	ds_read_b128 v[180:183], v149
	ds_read_b128 v[184:187], v150
	ds_read_b128 v[188:191], v151
	v_readfirstlane_b32 s49, v156
	v_lshl_add_u64 v[232:233], v[192:193], 0, s[38:39]
	s_mov_b32 m0, s49
	v_readfirstlane_b32 s49, v157
	ds_read_b128 v[196:199], v173 offset:32768
	ds_read_b128 v[200:203], v173 offset:33792
	ds_read_b128 v[204:207], v173 offset:34816
	ds_read_b128 v[212:215], v173 offset:35840
	ds_read_b128 v[216:219], v173 offset:36864
	ds_read_b128 v[220:223], v173 offset:37888
	ds_read_b128 v[224:227], v173 offset:38912
	ds_read_b128 v[228:231], v173 offset:39936
	global_load_lds_dwordx4 v[232:233], off
	v_lshl_add_u64 v[232:233], v[248:249], 0, s[38:39]
	s_mov_b32 m0, s49
	s_nop 0
	global_load_lds_dwordx4 v[232:233], off
	s_waitcnt lgkmcnt(8)
	s_barrier
	s_waitcnt lgkmcnt(0)
	v_mfma_f32_16x16x32_f16 v[2:5], v[196:199], v[176:179], v[2:5]
	v_mfma_f32_16x16x32_f16 v[6:9], v[196:199], v[184:187], v[6:9]
	v_mfma_f32_16x16x32_f16 v[10:13], v[204:207], v[176:179], v[10:13]
	v_mfma_f32_16x16x32_f16 v[18:21], v[204:207], v[184:187], v[18:21]
	v_mfma_f32_16x16x32_f16 v[30:33], v[216:219], v[176:179], v[30:33]
	v_mfma_f32_16x16x32_f16 v[42:45], v[216:219], v[184:187], v[42:45]
	v_mfma_f32_16x16x32_f16 v[54:57], v[224:227], v[176:179], v[54:57]
	v_mfma_f32_16x16x32_f16 v[66:69], v[224:227], v[184:187], v[66:69]
	v_mfma_f32_16x16x32_f16 v[2:5], v[200:203], v[180:183], v[2:5]
	v_mfma_f32_16x16x32_f16 v[6:9], v[200:203], v[188:191], v[6:9]
	v_mfma_f32_16x16x32_f16 v[10:13], v[212:215], v[180:183], v[10:13]
	v_mfma_f32_16x16x32_f16 v[18:21], v[212:215], v[188:191], v[18:21]
	v_mfma_f32_16x16x32_f16 v[30:33], v[220:223], v[180:183], v[30:33]
	v_mfma_f32_16x16x32_f16 v[42:45], v[220:223], v[188:191], v[42:45]
	v_mfma_f32_16x16x32_f16 v[54:57], v[228:231], v[180:183], v[54:57]
	v_mfma_f32_16x16x32_f16 v[66:69], v[228:231], v[188:191], v[66:69]
	s_barrier
	v_readfirstlane_b32 s49, v158
	v_lshl_add_u64 v[254:255], v[250:251], 0, s[40:41]
	s_mov_b32 m0, s49
	v_readfirstlane_b32 s49, v159
	ds_read_b128 v[232:235], v142
	ds_read_b128 v[236:239], v143
	ds_read_b128 v[240:243], v144
	ds_read_b128 v[244:247], v145
	global_load_lds_dwordx4 v[254:255], off
	v_lshl_add_u64 v[254:255], v[252:253], 0, s[40:41]
	s_mov_b32 m0, s49
	s_nop 0
	global_load_lds_dwordx4 v[254:255], off
	s_barrier
	s_waitcnt lgkmcnt(0)
	v_mfma_f32_16x16x32_f16 v[14:17], v[196:199], v[232:235], v[14:17]
	v_mfma_f32_16x16x32_f16 v[22:25], v[196:199], v[240:243], v[22:25]
	v_mfma_f32_16x16x32_f16 v[34:37], v[204:207], v[232:235], v[34:37]
	v_mfma_f32_16x16x32_f16 v[46:49], v[204:207], v[240:243], v[46:49]
	v_mfma_f32_16x16x32_f16 v[58:61], v[216:219], v[232:235], v[58:61]
	v_mfma_f32_16x16x32_f16 v[70:73], v[216:219], v[240:243], v[70:73]
	v_mfma_f32_16x16x32_f16 v[78:81], v[224:227], v[232:235], v[78:81]
	v_mfma_f32_16x16x32_f16 v[86:89], v[224:227], v[240:243], v[86:89]
	v_mfma_f32_16x16x32_f16 v[14:17], v[200:203], v[236:239], v[14:17]
	v_mfma_f32_16x16x32_f16 v[22:25], v[200:203], v[244:247], v[22:25]
	v_mfma_f32_16x16x32_f16 v[34:37], v[212:215], v[236:239], v[34:37]
	v_mfma_f32_16x16x32_f16 v[46:49], v[212:215], v[244:247], v[46:49]
	v_mfma_f32_16x16x32_f16 v[58:61], v[220:223], v[236:239], v[58:61]
	v_mfma_f32_16x16x32_f16 v[70:73], v[220:223], v[244:247], v[70:73]
	v_mfma_f32_16x16x32_f16 v[78:81], v[228:231], v[236:239], v[78:81]
	v_mfma_f32_16x16x32_f16 v[86:89], v[228:231], v[244:247], v[86:89]
	v_readfirstlane_b32 s49, v160
	v_lshl_add_u64 v[192:193], v[192:193], 0, s[40:41]
	s_mov_b32 m0, s49
	v_readfirstlane_b32 s49, v165
	s_barrier
	ds_read_b128 v[196:199], v173 offset:49152
	ds_read_b128 v[200:203], v173 offset:50176
	ds_read_b128 v[204:207], v173 offset:51200
	ds_read_b128 v[212:215], v173 offset:52224
	ds_read_b128 v[216:219], v173 offset:53248
	ds_read_b128 v[220:223], v173 offset:54272
	ds_read_b128 v[224:227], v173 offset:55296
	ds_read_b128 v[228:231], v173 offset:56320
	global_load_lds_dwordx4 v[192:193], off
	v_lshl_add_u64 v[192:193], v[248:249], 0, s[40:41]
	s_mov_b32 m0, s49
	s_nop 0
	global_load_lds_dwordx4 v[192:193], off
	s_barrier
	s_waitcnt lgkmcnt(0)
	v_mfma_f32_16x16x32_f16 v[26:29], v[196:199], v[176:179], v[26:29]
	v_mfma_f32_16x16x32_f16 v[38:41], v[196:199], v[184:187], v[38:41]
	v_mfma_f32_16x16x32_f16 v[50:53], v[204:207], v[176:179], v[50:53]
	v_mfma_f32_16x16x32_f16 v[62:65], v[204:207], v[184:187], v[62:65]
	v_mfma_f32_16x16x32_f16 v[74:77], v[216:219], v[176:179], v[74:77]
	v_mfma_f32_16x16x32_f16 v[82:85], v[216:219], v[184:187], v[82:85]
	v_mfma_f32_16x16x32_f16 v[90:93], v[224:227], v[176:179], v[90:93]
	v_mfma_f32_16x16x32_f16 v[94:97], v[224:227], v[184:187], v[94:97]
	v_mfma_f32_16x16x32_f16 v[26:29], v[200:203], v[180:183], v[26:29]
	v_mfma_f32_16x16x32_f16 v[38:41], v[200:203], v[188:191], v[38:41]
	v_mfma_f32_16x16x32_f16 v[50:53], v[212:215], v[180:183], v[50:53]
	v_mfma_f32_16x16x32_f16 v[62:65], v[212:215], v[188:191], v[62:65]
	v_mfma_f32_16x16x32_f16 v[74:77], v[220:223], v[180:183], v[74:77]
	v_mfma_f32_16x16x32_f16 v[82:85], v[220:223], v[188:191], v[82:85]
	v_mfma_f32_16x16x32_f16 v[90:93], v[228:231], v[180:183], v[90:93]
	v_mfma_f32_16x16x32_f16 v[94:97], v[228:231], v[188:191], v[94:97]
	s_barrier
	v_readfirstlane_b32 s49, v166
	v_lshl_add_u64 v[176:177], v[250:251], 0, s[42:43]
	s_mov_b32 m0, s49
	v_readfirstlane_b32 s49, v167
	global_load_lds_dwordx4 v[176:177], off
	v_lshl_add_u64 v[176:177], v[252:253], 0, s[42:43]
	s_mov_b32 m0, s49
	s_nop 0
	global_load_lds_dwordx4 v[176:177], off
	s_waitcnt vmcnt(6)
	s_barrier
	v_mfma_f32_16x16x32_f16 v[98:101], v[196:199], v[232:235], v[98:101]
	v_mfma_f32_16x16x32_f16 v[102:105], v[196:199], v[240:243], v[102:105]
	v_mfma_f32_16x16x32_f16 v[106:109], v[204:207], v[232:235], v[106:109]
	v_mfma_f32_16x16x32_f16 v[110:113], v[204:207], v[240:243], v[110:113]
	v_mfma_f32_16x16x32_f16 v[114:117], v[216:219], v[232:235], v[114:117]
	v_mfma_f32_16x16x32_f16 v[118:121], v[216:219], v[240:243], v[118:121]
	v_mfma_f32_16x16x32_f16 v[122:125], v[224:227], v[232:235], v[122:125]
	v_mfma_f32_16x16x32_f16 v[126:129], v[224:227], v[240:243], v[126:129]
	v_mfma_f32_16x16x32_f16 v[98:101], v[200:203], v[236:239], v[98:101]
	v_mfma_f32_16x16x32_f16 v[102:105], v[200:203], v[244:247], v[102:105]
	v_mfma_f32_16x16x32_f16 v[106:109], v[212:215], v[236:239], v[106:109]
	v_mfma_f32_16x16x32_f16 v[110:113], v[212:215], v[244:247], v[110:113]
	v_mfma_f32_16x16x32_f16 v[114:117], v[220:223], v[236:239], v[114:117]
	v_mfma_f32_16x16x32_f16 v[118:121], v[220:223], v[244:247], v[118:121]
	v_mfma_f32_16x16x32_f16 v[122:125], v[228:231], v[236:239], v[122:125]
	v_mfma_f32_16x16x32_f16 v[126:129], v[228:231], v[244:247], v[126:129]
	s_add_i32 s48, s48, 2
	s_add_u32 s46, s46, 0x100
	s_addc_u32 s47, s47, 0
	s_cmp_lt_u32 s48, 4
	s_barrier
	s_cbranch_scc1 .LBB7_239
	s_add_u32 s0, s0, 0x20380
	s_addc_u32 s1, s1, 0
	v_readfirstlane_b32 s5, v174
	v_lshl_add_u64 v[130:131], v[130:131], 1, s[0:1]
	s_mov_b32 m0, s5
	ds_read_b128 v[134:137], v169
	ds_read_b128 v[138:141], v170
	ds_read_b128 v[152:155], v171
	ds_read_b128 v[156:159], v172
	ds_read_b128 v[166:169], v173
	ds_read_b128 v[176:179], v173 offset:1024
	ds_read_b128 v[180:183], v173 offset:2048
	ds_read_b128 v[184:187], v173 offset:3072
	ds_read_b128 v[188:191], v173 offset:4096
	ds_read_b128 v[196:199], v173 offset:5120
	ds_read_b128 v[200:203], v173 offset:6144
	ds_read_b128 v[204:207], v173 offset:7168
	global_load_lds_dwordx4 v[130:131], off
	v_lshl_add_u64 v[130:131], v[132:133], 1, s[0:1]
	v_readfirstlane_b32 s0, v175
	s_mov_b32 m0, s0
	s_nop 0
	global_load_lds_dwordx4 v[130:131], off
	s_barrier
	s_waitcnt lgkmcnt(0)
	v_mfma_f32_16x16x32_f16 v[2:5], v[166:169], v[134:137], v[2:5]
	v_mfma_f32_16x16x32_f16 v[42:45], v[188:191], v[152:155], v[42:45]
	v_mfma_f32_16x16x32_f16 v[54:57], v[200:203], v[134:137], v[54:57]
	v_mfma_f32_16x16x32_f16 v[66:69], v[200:203], v[152:155], v[66:69]
	v_mfma_f32_16x16x32_f16 v[2:5], v[176:179], v[138:141], v[2:5]
	v_mfma_f32_16x16x32_f16 v[6:9], v[166:169], v[152:155], v[6:9]
	v_mfma_f32_16x16x32_f16 v[10:13], v[180:183], v[134:137], v[10:13]
	v_mfma_f32_16x16x32_f16 v[18:21], v[180:183], v[152:155], v[18:21]
	v_mfma_f32_16x16x32_f16 v[30:33], v[188:191], v[134:137], v[30:33]
	v_mfma_f32_16x16x32_f16 v[42:45], v[196:199], v[156:159], v[42:45]
	v_mfma_f32_16x16x32_f16 v[54:57], v[204:207], v[138:141], v[54:57]
	v_mfma_f32_16x16x32_f16 v[66:69], v[204:207], v[156:159], v[66:69]
	v_mfma_f32_16x16x32_f16 v[6:9], v[176:179], v[156:159], v[6:9]
	v_mfma_f32_16x16x32_f16 v[10:13], v[184:187], v[138:141], v[10:13]
	v_mfma_f32_16x16x32_f16 v[18:21], v[184:187], v[156:159], v[18:21]
	v_mfma_f32_16x16x32_f16 v[30:33], v[196:199], v[138:141], v[30:33]
	s_barrier
	ds_read_b128 v[130:133], v161
	ds_read_b128 v[212:215], v162
	ds_read_b128 v[160:163], v163
	ds_read_b128 v[216:219], v164
	s_barrier
	s_waitcnt lgkmcnt(0)
	v_mfma_f32_16x16x32_f16 v[14:17], v[166:169], v[130:133], v[14:17]
	v_mfma_f32_16x16x32_f16 v[78:81], v[200:203], v[130:133], v[78:81]
	v_mfma_f32_16x16x32_f16 v[14:17], v[176:179], v[212:215], v[14:17]
	v_mfma_f32_16x16x32_f16 v[22:25], v[166:169], v[160:163], v[22:25]
	v_mfma_f32_16x16x32_f16 v[34:37], v[180:183], v[130:133], v[34:37]
	v_mfma_f32_16x16x32_f16 v[46:49], v[180:183], v[160:163], v[46:49]
	v_mfma_f32_16x16x32_f16 v[58:61], v[188:191], v[130:133], v[58:61]
	v_mfma_f32_16x16x32_f16 v[70:73], v[188:191], v[160:163], v[70:73]
	v_mfma_f32_16x16x32_f16 v[164:167], v[204:207], v[212:215], v[78:81]
	v_mfma_f32_16x16x32_f16 v[78:81], v[200:203], v[160:163], v[86:89]
	v_mfma_f32_16x16x32_f16 v[22:25], v[176:179], v[216:219], v[22:25]
	v_mfma_f32_16x16x32_f16 v[34:37], v[184:187], v[212:215], v[34:37]
	v_mfma_f32_16x16x32_f16 v[46:49], v[184:187], v[216:219], v[46:49]
	v_mfma_f32_16x16x32_f16 v[58:61], v[196:199], v[212:215], v[58:61]
	v_mfma_f32_16x16x32_f16 v[70:73], v[196:199], v[216:219], v[70:73]
	v_mfma_f32_16x16x32_f16 v[86:89], v[204:207], v[216:219], v[78:81]
	s_barrier
	s_nop 0
	ds_read_b128 v[78:81], v173 offset:16384
	ds_read_b128 v[168:171], v173 offset:17408
	ds_read_b128 v[174:177], v173 offset:18432
	ds_read_b128 v[178:181], v173 offset:19456
	ds_read_b128 v[182:185], v173 offset:20480
	ds_read_b128 v[186:189], v173 offset:21504
	ds_read_b128 v[190:193], v173 offset:22528
	ds_read_b128 v[196:199], v173 offset:23552
	s_waitcnt vmcnt(4)
	s_barrier
	s_waitcnt lgkmcnt(0)
	v_mfma_f32_16x16x32_f16 v[26:29], v[78:81], v[134:137], v[26:29]
	v_mfma_f32_16x16x32_f16 v[38:41], v[78:81], v[152:155], v[38:41]
	v_mfma_f32_16x16x32_f16 v[26:29], v[168:171], v[138:141], v[26:29]
	v_mfma_f32_16x16x32_f16 v[38:41], v[168:171], v[156:159], v[38:41]
	v_mfma_f32_16x16x32_f16 v[50:53], v[174:177], v[134:137], v[50:53]
	v_mfma_f32_16x16x32_f16 v[62:65], v[174:177], v[152:155], v[62:65]
	v_mfma_f32_16x16x32_f16 v[74:77], v[182:185], v[134:137], v[74:77]
	v_mfma_f32_16x16x32_f16 v[82:85], v[182:185], v[152:155], v[82:85]
	v_mfma_f32_16x16x32_f16 v[90:93], v[190:193], v[134:137], v[90:93]
	v_mfma_f32_16x16x32_f16 v[94:97], v[190:193], v[152:155], v[94:97]
	v_mfma_f32_16x16x32_f16 v[50:53], v[178:181], v[138:141], v[50:53]
	v_mfma_f32_16x16x32_f16 v[62:65], v[178:181], v[156:159], v[62:65]
	v_mfma_f32_16x16x32_f16 v[74:77], v[186:189], v[138:141], v[74:77]
	v_mfma_f32_16x16x32_f16 v[82:85], v[186:189], v[156:159], v[82:85]
	v_mfma_f32_16x16x32_f16 v[90:93], v[196:199], v[138:141], v[90:93]
	v_mfma_f32_16x16x32_f16 v[94:97], v[196:199], v[156:159], v[94:97]
	v_mfma_f32_16x16x32_f16 v[98:101], v[78:81], v[130:133], v[98:101]
	v_mfma_f32_16x16x32_f16 v[78:81], v[78:81], v[160:163], v[102:105]
	v_mfma_f32_16x16x32_f16 v[102:105], v[168:171], v[216:219], v[78:81]
	v_mfma_f32_16x16x32_f16 v[78:81], v[174:177], v[130:133], v[106:109]
	v_mfma_f32_16x16x32_f16 v[106:109], v[178:181], v[212:215], v[78:81]
	v_mfma_f32_16x16x32_f16 v[78:81], v[174:177], v[160:163], v[110:113]
	v_mfma_f32_16x16x32_f16 v[200:203], v[178:181], v[216:219], v[78:81]
	v_mfma_f32_16x16x32_f16 v[78:81], v[182:185], v[130:133], v[114:117]
	v_mfma_f32_16x16x32_f16 v[204:207], v[186:189], v[212:215], v[78:81]
	v_mfma_f32_16x16x32_f16 v[78:81], v[182:185], v[160:163], v[118:121]
	v_mfma_f32_16x16x32_f16 v[220:223], v[186:189], v[216:219], v[78:81]
	v_mfma_f32_16x16x32_f16 v[78:81], v[190:193], v[130:133], v[122:125]
	v_mfma_f32_16x16x32_f16 v[98:101], v[168:171], v[212:215], v[98:101]
	v_mfma_f32_16x16x32_f16 v[212:215], v[196:199], v[212:215], v[78:81]
	v_mfma_f32_16x16x32_f16 v[78:81], v[190:193], v[160:163], v[126:129]
	v_mfma_f32_16x16x32_f16 v[196:199], v[196:199], v[216:219], v[78:81]
	s_barrier
	ds_read_b128 v[110:113], v148
	ds_read_b128 v[130:133], v149
	ds_read_b128 v[216:219], v150
	ds_read_b128 v[224:227], v151
	s_nop 0
	ds_read_b128 v[78:81], v173 offset:32768
	ds_read_b128 v[114:117], v173 offset:33792
	ds_read_b128 v[118:121], v173 offset:34816
	ds_read_b128 v[134:137], v173 offset:35840
	ds_read_b128 v[138:141], v173 offset:36864
	ds_read_b128 v[168:171], v173 offset:37888
	ds_read_b128 v[174:177], v173 offset:38912
	ds_read_b128 v[228:231], v173 offset:39936
	s_waitcnt vmcnt(2)
	s_barrier
	s_waitcnt lgkmcnt(0)
	v_mfma_f32_16x16x32_f16 v[2:5], v[78:81], v[110:113], v[2:5]
	v_mfma_f32_16x16x32_f16 v[190:193], v[114:117], v[130:133], v[2:5]
	v_mfma_f32_16x16x32_f16 v[2:5], v[78:81], v[216:219], v[6:9]
	v_mfma_f32_16x16x32_f16 v[158:161], v[114:117], v[224:227], v[2:5]
	v_mfma_f32_16x16x32_f16 v[2:5], v[118:121], v[110:113], v[10:13]
	v_mfma_f32_16x16x32_f16 v[186:189], v[134:137], v[130:133], v[2:5]
	v_mfma_f32_16x16x32_f16 v[2:5], v[118:121], v[216:219], v[18:21]
	v_mfma_f32_16x16x32_f16 v[154:157], v[134:137], v[224:227], v[2:5]
	v_mfma_f32_16x16x32_f16 v[2:5], v[138:141], v[110:113], v[30:33]
	v_mfma_f32_16x16x32_f16 v[182:185], v[168:171], v[130:133], v[2:5]
	v_mfma_f32_16x16x32_f16 v[2:5], v[138:141], v[216:219], v[42:45]
	v_mfma_f32_16x16x32_f16 v[150:153], v[168:171], v[224:227], v[2:5]
	v_mfma_f32_16x16x32_f16 v[2:5], v[174:177], v[110:113], v[54:57]
	v_mfma_f32_16x16x32_f16 v[178:181], v[228:231], v[130:133], v[2:5]
	v_mfma_f32_16x16x32_f16 v[2:5], v[174:177], v[216:219], v[66:69]
	v_mfma_f32_16x16x32_f16 v[146:149], v[228:231], v[224:227], v[2:5]
	s_barrier
	s_nop 4
	ds_read_b128 v[2:5], v142
	ds_read_b128 v[6:9], v143
	ds_read_b128 v[10:13], v144
	ds_read_b128 v[18:21], v145
	s_waitcnt vmcnt(0)
	s_barrier
	s_waitcnt lgkmcnt(0)
	v_mfma_f32_16x16x32_f16 v[14:17], v[78:81], v[2:5], v[14:17]
	v_mfma_f32_16x16x32_f16 v[126:129], v[114:117], v[6:9], v[14:17]
	v_mfma_f32_16x16x32_f16 v[14:17], v[78:81], v[10:13], v[22:25]
	v_mfma_f32_16x16x32_f16 v[78:81], v[114:117], v[18:21], v[14:17]
	v_mfma_f32_16x16x32_f16 v[14:17], v[118:121], v[2:5], v[34:37]
	v_mfma_f32_16x16x32_f16 v[122:125], v[134:137], v[6:9], v[14:17]
	v_mfma_f32_16x16x32_f16 v[14:17], v[118:121], v[10:13], v[46:49]
	v_mfma_f32_16x16x32_f16 v[66:69], v[134:137], v[18:21], v[14:17]
	v_mfma_f32_16x16x32_f16 v[14:17], v[138:141], v[2:5], v[58:61]
	v_mfma_f32_16x16x32_f16 v[118:121], v[168:171], v[6:9], v[14:17]
	v_mfma_f32_16x16x32_f16 v[14:17], v[138:141], v[10:13], v[70:73]
	v_mfma_f32_16x16x32_f16 v[54:57], v[168:171], v[18:21], v[14:17]
	v_mfma_f32_16x16x32_f16 v[14:17], v[174:177], v[2:5], v[164:167]
	v_mfma_f32_16x16x32_f16 v[114:117], v[228:231], v[6:9], v[14:17]
	v_mfma_f32_16x16x32_f16 v[14:17], v[174:177], v[10:13], v[86:89]
	v_mfma_f32_16x16x32_f16 v[42:45], v[228:231], v[18:21], v[14:17]
	s_barrier
	s_nop 4
	ds_read_b128 v[14:17], v173 offset:49152
	ds_read_b128 v[22:25], v173 offset:50176
	ds_read_b128 v[30:33], v173 offset:51200
	ds_read_b128 v[34:37], v173 offset:52224
	ds_read_b128 v[46:49], v173 offset:53248
	ds_read_b128 v[58:61], v173 offset:54272
	ds_read_b128 v[70:73], v173 offset:55296
	ds_read_b128 v[86:89], v173 offset:56320
	s_barrier
	s_waitcnt lgkmcnt(0)
	v_mfma_f32_16x16x32_f16 v[26:29], v[14:17], v[110:113], v[26:29]
	v_mfma_f32_16x16x32_f16 v[174:177], v[22:25], v[130:133], v[26:29]
	v_mfma_f32_16x16x32_f16 v[26:29], v[14:17], v[216:219], v[38:41]
	v_mfma_f32_16x16x32_f16 v[142:145], v[22:25], v[224:227], v[26:29]
	v_mfma_f32_16x16x32_f16 v[26:29], v[30:33], v[110:113], v[50:53]
	v_mfma_f32_16x16x32_f16 v[170:173], v[34:37], v[130:133], v[26:29]
	v_mfma_f32_16x16x32_f16 v[26:29], v[30:33], v[216:219], v[62:65]
	v_mfma_f32_16x16x32_f16 v[138:141], v[34:37], v[224:227], v[26:29]
	v_mfma_f32_16x16x32_f16 v[26:29], v[46:49], v[110:113], v[74:77]
	v_mfma_f32_16x16x32_f16 v[166:169], v[58:61], v[130:133], v[26:29]
	v_mfma_f32_16x16x32_f16 v[26:29], v[46:49], v[216:219], v[82:85]
	v_mfma_f32_16x16x32_f16 v[134:137], v[58:61], v[224:227], v[26:29]
	v_mfma_f32_16x16x32_f16 v[26:29], v[70:73], v[110:113], v[90:93]
	v_mfma_f32_16x16x32_f16 v[162:165], v[86:89], v[130:133], v[26:29]
	v_mfma_f32_16x16x32_f16 v[26:29], v[70:73], v[216:219], v[94:97]
	v_mfma_f32_16x16x32_f16 v[130:133], v[86:89], v[224:227], v[26:29]
	v_mfma_f32_16x16x32_f16 v[26:29], v[14:17], v[2:5], v[98:101]
	v_mfma_f32_16x16x32_f16 v[14:17], v[14:17], v[10:13], v[102:105]
	v_mfma_f32_16x16x32_f16 v[38:41], v[22:25], v[18:21], v[14:17]
	v_mfma_f32_16x16x32_f16 v[14:17], v[30:33], v[2:5], v[106:109]
	v_mfma_f32_16x16x32_f16 v[106:109], v[34:37], v[6:9], v[14:17]
	v_mfma_f32_16x16x32_f16 v[14:17], v[30:33], v[10:13], v[200:203]
	v_mfma_f32_16x16x32_f16 v[110:113], v[22:25], v[6:9], v[26:29]
	v_mfma_f32_16x16x32_f16 v[26:29], v[34:37], v[18:21], v[14:17]
	v_mfma_f32_16x16x32_f16 v[14:17], v[46:49], v[2:5], v[204:207]
	v_mfma_f32_16x16x32_f16 v[2:5], v[70:73], v[2:5], v[212:215]
	v_mfma_f32_16x16x32_f16 v[102:105], v[58:61], v[6:9], v[14:17]
	v_mfma_f32_16x16x32_f16 v[14:17], v[46:49], v[10:13], v[220:223]
	v_mfma_f32_16x16x32_f16 v[98:101], v[86:89], v[6:9], v[2:5]
	v_mfma_f32_16x16x32_f16 v[2:5], v[70:73], v[10:13], v[196:199]
	v_mfma_f32_16x16x32_f16 v[14:17], v[58:61], v[18:21], v[14:17]
	v_mfma_f32_16x16x32_f16 v[2:5], v[86:89], v[18:21], v[2:5]
	s_cmpk_gt_u32 s65, 0xff
	s_barrier
	s_cbranch_scc1 .LBB7_242
	s_barrier

.LBB8_41:
	ds_read_b128 v[182:185], v171
	ds_read_b128 v[186:189], v173
	ds_read_b128 v[190:193], v174
	ds_read_b128 v[194:197], v175
	v_add_u32_e32 v177, 0xc000, v148
	v_lshl_add_u64 v[246:247], v[134:135], 0, s[44:45]
	v_readfirstlane_b32 s47, v177
	v_add_u32_e32 v176, s48, v170
	v_lshl_add_u64 v[178:179], v[246:247], 0, s[28:29]
	s_mov_b32 m0, s47
	ds_read_b128 v[198:201], v176
	ds_read_b128 v[202:205], v176 offset:1024
	ds_read_b128 v[206:209], v176 offset:2048
	ds_read_b128 v[210:213], v176 offset:3072
	ds_read_b128 v[214:217], v176 offset:4096
	ds_read_b128 v[218:221], v176 offset:5120
	ds_read_b128 v[222:225], v176 offset:6144
	ds_read_b128 v[226:229], v176 offset:7168
	global_load_lds_dwordx4 v[178:179], off
	v_add_u32_e32 v178, 0xe000, v148
	v_lshl_add_u64 v[248:249], v[136:137], 0, s[44:45]
	v_readfirstlane_b32 s47, v178
	v_lshl_add_u64 v[230:231], v[248:249], 0, s[28:29]
	s_mov_b32 m0, s47
	s_nop 0
	global_load_lds_dwordx4 v[230:231], off
	s_waitcnt lgkmcnt(8)
	s_barrier
	s_waitcnt lgkmcnt(0)
	v_mfma_f32_16x16x32_f16 v[126:129], v[198:201], v[182:185], v[126:129]
	v_mfma_f32_16x16x32_f16 v[122:125], v[198:201], v[190:193], v[122:125]
	v_mfma_f32_16x16x32_f16 v[118:121], v[206:209], v[182:185], v[118:121]
	v_mfma_f32_16x16x32_f16 v[114:117], v[206:209], v[190:193], v[114:117]
	v_mfma_f32_16x16x32_f16 v[110:113], v[214:217], v[182:185], v[110:113]
	v_mfma_f32_16x16x32_f16 v[106:109], v[214:217], v[190:193], v[106:109]
	v_mfma_f32_16x16x32_f16 v[102:105], v[222:225], v[182:185], v[102:105]
	v_mfma_f32_16x16x32_f16 v[98:101], v[222:225], v[190:193], v[98:101]
	v_mfma_f32_16x16x32_f16 v[126:129], v[202:205], v[186:189], v[126:129]
	v_mfma_f32_16x16x32_f16 v[122:125], v[202:205], v[194:197], v[122:125]
	v_mfma_f32_16x16x32_f16 v[118:121], v[210:213], v[186:189], v[118:121]
	v_mfma_f32_16x16x32_f16 v[114:117], v[210:213], v[194:197], v[114:117]
	v_mfma_f32_16x16x32_f16 v[110:113], v[218:221], v[186:189], v[110:113]
	v_mfma_f32_16x16x32_f16 v[106:109], v[218:221], v[194:197], v[106:109]
	v_mfma_f32_16x16x32_f16 v[102:105], v[226:229], v[186:189], v[102:105]
	v_mfma_f32_16x16x32_f16 v[98:101], v[226:229], v[194:197], v[98:101]
	s_barrier
	v_lshl_add_u64 v[250:251], v[138:139], 0, s[44:45]
	v_readfirstlane_b32 s47, v142
	v_lshl_add_u64 v[252:253], v[250:251], 0, s[30:31]
	s_mov_b32 m0, s47
	ds_read_b128 v[230:233], v162
	ds_read_b128 v[234:237], v163
	ds_read_b128 v[238:241], v164
	ds_read_b128 v[242:245], v165
	global_load_lds_dwordx4 v[252:253], off
	v_lshl_add_u64 v[252:253], v[140:141], 0, s[44:45]
	v_readfirstlane_b32 s47, v143
	v_lshl_add_u64 v[254:255], v[252:253], 0, s[30:31]
	s_mov_b32 m0, s47
	s_nop 0
	global_load_lds_dwordx4 v[254:255], off
	s_barrier
	s_waitcnt lgkmcnt(0)
	v_mfma_f32_16x16x32_f16 v[94:97], v[198:201], v[230:233], v[94:97]
	v_mfma_f32_16x16x32_f16 v[90:93], v[198:201], v[238:241], v[90:93]
	v_mfma_f32_16x16x32_f16 v[86:89], v[206:209], v[230:233], v[86:89]
	v_mfma_f32_16x16x32_f16 v[82:85], v[206:209], v[238:241], v[82:85]
	v_mfma_f32_16x16x32_f16 v[78:81], v[214:217], v[230:233], v[78:81]
	v_mfma_f32_16x16x32_f16 v[74:77], v[214:217], v[238:241], v[74:77]
	v_mfma_f32_16x16x32_f16 v[70:73], v[222:225], v[230:233], v[70:73]
	v_mfma_f32_16x16x32_f16 v[66:69], v[222:225], v[238:241], v[66:69]
	v_mfma_f32_16x16x32_f16 v[94:97], v[202:205], v[234:237], v[94:97]
	v_mfma_f32_16x16x32_f16 v[90:93], v[202:205], v[242:245], v[90:93]
	v_mfma_f32_16x16x32_f16 v[86:89], v[210:213], v[234:237], v[86:89]
	v_mfma_f32_16x16x32_f16 v[82:85], v[210:213], v[242:245], v[82:85]
	v_mfma_f32_16x16x32_f16 v[78:81], v[218:221], v[234:237], v[78:81]
	v_mfma_f32_16x16x32_f16 v[74:77], v[218:221], v[242:245], v[74:77]
	v_mfma_f32_16x16x32_f16 v[70:73], v[226:229], v[234:237], v[70:73]
	v_mfma_f32_16x16x32_f16 v[66:69], v[226:229], v[242:245], v[66:69]
	v_readfirstlane_b32 s47, v148
	v_lshl_add_u64 v[254:255], v[246:247], 0, s[30:31]
	s_mov_b32 m0, s47
	v_readfirstlane_b32 s47, v149
	s_barrier
	ds_read_b128 v[198:201], v176 offset:16384
	ds_read_b128 v[202:205], v176 offset:17408
	ds_read_b128 v[206:209], v176 offset:18432
	ds_read_b128 v[210:213], v176 offset:19456
	ds_read_b128 v[214:217], v176 offset:20480
	ds_read_b128 v[218:221], v176 offset:21504
	ds_read_b128 v[222:225], v176 offset:22528
	ds_read_b128 v[226:229], v176 offset:23552
	global_load_lds_dwordx4 v[254:255], off
	v_lshl_add_u64 v[254:255], v[248:249], 0, s[30:31]
	s_mov_b32 m0, s47
	s_nop 0
	global_load_lds_dwordx4 v[254:255], off
	s_barrier
	s_waitcnt lgkmcnt(0)
	v_mfma_f32_16x16x32_f16 v[62:65], v[198:201], v[182:185], v[62:65]
	v_mfma_f32_16x16x32_f16 v[58:61], v[198:201], v[190:193], v[58:61]
	v_mfma_f32_16x16x32_f16 v[54:57], v[206:209], v[182:185], v[54:57]
	v_mfma_f32_16x16x32_f16 v[50:53], v[206:209], v[190:193], v[50:53]
	v_mfma_f32_16x16x32_f16 v[46:49], v[214:217], v[182:185], v[46:49]
	v_mfma_f32_16x16x32_f16 v[42:45], v[214:217], v[190:193], v[42:45]
	v_mfma_f32_16x16x32_f16 v[38:41], v[222:225], v[182:185], v[38:41]
	v_mfma_f32_16x16x32_f16 v[34:37], v[222:225], v[190:193], v[34:37]
	v_mfma_f32_16x16x32_f16 v[62:65], v[202:205], v[186:189], v[62:65]
	v_mfma_f32_16x16x32_f16 v[58:61], v[202:205], v[194:197], v[58:61]
	v_mfma_f32_16x16x32_f16 v[54:57], v[210:213], v[186:189], v[54:57]
	v_mfma_f32_16x16x32_f16 v[50:53], v[210:213], v[194:197], v[50:53]
	v_mfma_f32_16x16x32_f16 v[46:49], v[218:221], v[186:189], v[46:49]
	v_mfma_f32_16x16x32_f16 v[42:45], v[218:221], v[194:197], v[42:45]
	v_mfma_f32_16x16x32_f16 v[38:41], v[226:229], v[186:189], v[38:41]
	v_mfma_f32_16x16x32_f16 v[34:37], v[226:229], v[194:197], v[34:37]
	s_barrier
	v_readfirstlane_b32 s47, v154
	v_lshl_add_u64 v[182:183], v[250:251], 0, s[34:35]
	s_mov_b32 m0, s47
	v_readfirstlane_b32 s47, v155
	global_load_lds_dwordx4 v[182:183], off
	v_lshl_add_u64 v[182:183], v[252:253], 0, s[34:35]
	s_mov_b32 m0, s47
	s_nop 0
	global_load_lds_dwordx4 v[182:183], off
	s_waitcnt vmcnt(6)
	s_barrier
	v_mfma_f32_16x16x32_f16 v[30:33], v[198:201], v[230:233], v[30:33]
	v_mfma_f32_16x16x32_f16 v[26:29], v[198:201], v[238:241], v[26:29]
	v_mfma_f32_16x16x32_f16 v[22:25], v[206:209], v[230:233], v[22:25]
	v_mfma_f32_16x16x32_f16 v[18:21], v[206:209], v[238:241], v[18:21]
	v_mfma_f32_16x16x32_f16 v[14:17], v[214:217], v[230:233], v[14:17]
	v_mfma_f32_16x16x32_f16 v[10:13], v[214:217], v[238:241], v[10:13]
	v_mfma_f32_16x16x32_f16 v[6:9], v[222:225], v[230:233], v[6:9]
	v_mfma_f32_16x16x32_f16 v[2:5], v[222:225], v[238:241], v[2:5]
	v_mfma_f32_16x16x32_f16 v[30:33], v[202:205], v[234:237], v[30:33]
	v_mfma_f32_16x16x32_f16 v[26:29], v[202:205], v[242:245], v[26:29]
	v_mfma_f32_16x16x32_f16 v[22:25], v[210:213], v[234:237], v[22:25]
	v_mfma_f32_16x16x32_f16 v[18:21], v[210:213], v[242:245], v[18:21]
	v_mfma_f32_16x16x32_f16 v[14:17], v[218:221], v[234:237], v[14:17]
	v_mfma_f32_16x16x32_f16 v[10:13], v[218:221], v[242:245], v[10:13]
	v_mfma_f32_16x16x32_f16 v[6:9], v[226:229], v[234:237], v[6:9]
	v_mfma_f32_16x16x32_f16 v[2:5], v[226:229], v[242:245], v[2:5]
	s_barrier
	ds_read_b128 v[182:185], v144
	ds_read_b128 v[186:189], v145
	ds_read_b128 v[190:193], v146
	ds_read_b128 v[194:197], v147
	v_readfirstlane_b32 s47, v156
	v_lshl_add_u64 v[230:231], v[246:247], 0, s[34:35]
	s_mov_b32 m0, s47
	v_readfirstlane_b32 s47, v157
	ds_read_b128 v[198:201], v176 offset:32768
	ds_read_b128 v[202:205], v176 offset:33792
	ds_read_b128 v[206:209], v176 offset:34816
	ds_read_b128 v[210:213], v176 offset:35840
	ds_read_b128 v[214:217], v176 offset:36864
	ds_read_b128 v[218:221], v176 offset:37888
	ds_read_b128 v[222:225], v176 offset:38912
	ds_read_b128 v[226:229], v176 offset:39936
	global_load_lds_dwordx4 v[230:231], off
	v_lshl_add_u64 v[230:231], v[248:249], 0, s[34:35]
	s_mov_b32 m0, s47
	s_nop 0
	global_load_lds_dwordx4 v[230:231], off
	s_waitcnt lgkmcnt(8)
	s_barrier
	s_waitcnt lgkmcnt(0)
	v_mfma_f32_16x16x32_f16 v[126:129], v[198:201], v[182:185], v[126:129]
	v_mfma_f32_16x16x32_f16 v[122:125], v[198:201], v[190:193], v[122:125]
	v_mfma_f32_16x16x32_f16 v[118:121], v[206:209], v[182:185], v[118:121]
	v_mfma_f32_16x16x32_f16 v[114:117], v[206:209], v[190:193], v[114:117]
	v_mfma_f32_16x16x32_f16 v[110:113], v[214:217], v[182:185], v[110:113]
	v_mfma_f32_16x16x32_f16 v[106:109], v[214:217], v[190:193], v[106:109]
	v_mfma_f32_16x16x32_f16 v[102:105], v[222:225], v[182:185], v[102:105]
	v_mfma_f32_16x16x32_f16 v[98:101], v[222:225], v[190:193], v[98:101]
	v_mfma_f32_16x16x32_f16 v[126:129], v[202:205], v[186:189], v[126:129]
	v_mfma_f32_16x16x32_f16 v[122:125], v[202:205], v[194:197], v[122:125]
	v_mfma_f32_16x16x32_f16 v[118:121], v[210:213], v[186:189], v[118:121]
	v_mfma_f32_16x16x32_f16 v[114:117], v[210:213], v[194:197], v[114:117]
	v_mfma_f32_16x16x32_f16 v[110:113], v[218:221], v[186:189], v[110:113]
	v_mfma_f32_16x16x32_f16 v[106:109], v[218:221], v[194:197], v[106:109]
	v_mfma_f32_16x16x32_f16 v[102:105], v[226:229], v[186:189], v[102:105]
	v_mfma_f32_16x16x32_f16 v[98:101], v[226:229], v[194:197], v[98:101]
	s_barrier
	v_readfirstlane_b32 s47, v158
	v_lshl_add_u64 v[254:255], v[250:251], 0, s[36:37]
	s_mov_b32 m0, s47
	v_readfirstlane_b32 s47, v160
	ds_read_b128 v[230:233], v150
	ds_read_b128 v[234:237], v151
	ds_read_b128 v[238:241], v152
	ds_read_b128 v[242:245], v153
	global_load_lds_dwordx4 v[254:255], off
	v_lshl_add_u64 v[254:255], v[252:253], 0, s[36:37]
	s_mov_b32 m0, s47
	s_nop 0
	global_load_lds_dwordx4 v[254:255], off
	s_barrier
	s_waitcnt lgkmcnt(0)
	v_mfma_f32_16x16x32_f16 v[94:97], v[198:201], v[230:233], v[94:97]
	v_mfma_f32_16x16x32_f16 v[90:93], v[198:201], v[238:241], v[90:93]
	v_mfma_f32_16x16x32_f16 v[86:89], v[206:209], v[230:233], v[86:89]
	v_mfma_f32_16x16x32_f16 v[82:85], v[206:209], v[238:241], v[82:85]
	v_mfma_f32_16x16x32_f16 v[78:81], v[214:217], v[230:233], v[78:81]
	v_mfma_f32_16x16x32_f16 v[74:77], v[214:217], v[238:241], v[74:77]
	v_mfma_f32_16x16x32_f16 v[70:73], v[222:225], v[230:233], v[70:73]
	v_mfma_f32_16x16x32_f16 v[66:69], v[222:225], v[238:241], v[66:69]
	v_mfma_f32_16x16x32_f16 v[94:97], v[202:205], v[234:237], v[94:97]
	v_mfma_f32_16x16x32_f16 v[90:93], v[202:205], v[242:245], v[90:93]
	v_mfma_f32_16x16x32_f16 v[86:89], v[210:213], v[234:237], v[86:89]
	v_mfma_f32_16x16x32_f16 v[82:85], v[210:213], v[242:245], v[82:85]
	v_mfma_f32_16x16x32_f16 v[78:81], v[218:221], v[234:237], v[78:81]
	v_mfma_f32_16x16x32_f16 v[74:77], v[218:221], v[242:245], v[74:77]
	v_mfma_f32_16x16x32_f16 v[70:73], v[226:229], v[234:237], v[70:73]
	v_mfma_f32_16x16x32_f16 v[66:69], v[226:229], v[242:245], v[66:69]
	v_readfirstlane_b32 s47, v161
	v_lshl_add_u64 v[246:247], v[246:247], 0, s[36:37]
	s_mov_b32 m0, s47
	v_readfirstlane_b32 s47, v166
	s_barrier
	ds_read_b128 v[198:201], v176 offset:49152
	ds_read_b128 v[202:205], v176 offset:50176
	ds_read_b128 v[206:209], v176 offset:51200
	ds_read_b128 v[210:213], v176 offset:52224
	ds_read_b128 v[214:217], v176 offset:53248
	ds_read_b128 v[218:221], v176 offset:54272
	ds_read_b128 v[222:225], v176 offset:55296
	ds_read_b128 v[226:229], v176 offset:56320
	global_load_lds_dwordx4 v[246:247], off
	v_lshl_add_u64 v[246:247], v[248:249], 0, s[36:37]
	s_mov_b32 m0, s47
	s_nop 0
	global_load_lds_dwordx4 v[246:247], off
	s_barrier
	s_waitcnt lgkmcnt(0)
	v_mfma_f32_16x16x32_f16 v[62:65], v[198:201], v[182:185], v[62:65]
	v_mfma_f32_16x16x32_f16 v[58:61], v[198:201], v[190:193], v[58:61]
	v_mfma_f32_16x16x32_f16 v[54:57], v[206:209], v[182:185], v[54:57]
	v_mfma_f32_16x16x32_f16 v[50:53], v[206:209], v[190:193], v[50:53]
	v_mfma_f32_16x16x32_f16 v[46:49], v[214:217], v[182:185], v[46:49]
	v_mfma_f32_16x16x32_f16 v[42:45], v[214:217], v[190:193], v[42:45]
	v_mfma_f32_16x16x32_f16 v[38:41], v[222:225], v[182:185], v[38:41]
	v_mfma_f32_16x16x32_f16 v[34:37], v[222:225], v[190:193], v[34:37]
	v_mfma_f32_16x16x32_f16 v[62:65], v[202:205], v[186:189], v[62:65]
	v_mfma_f32_16x16x32_f16 v[58:61], v[202:205], v[194:197], v[58:61]
	v_mfma_f32_16x16x32_f16 v[54:57], v[210:213], v[186:189], v[54:57]
	v_mfma_f32_16x16x32_f16 v[50:53], v[210:213], v[194:197], v[50:53]
	v_mfma_f32_16x16x32_f16 v[46:49], v[218:221], v[186:189], v[46:49]
	v_mfma_f32_16x16x32_f16 v[42:45], v[218:221], v[194:197], v[42:45]
	v_mfma_f32_16x16x32_f16 v[38:41], v[226:229], v[186:189], v[38:41]
	v_mfma_f32_16x16x32_f16 v[34:37], v[226:229], v[194:197], v[34:37]
	s_barrier
	v_readfirstlane_b32 s47, v168
	v_lshl_add_u64 v[182:183], v[250:251], 0, s[38:39]
	s_mov_b32 m0, s47
	v_readfirstlane_b32 s47, v169
	global_load_lds_dwordx4 v[182:183], off
	v_lshl_add_u64 v[182:183], v[252:253], 0, s[38:39]
	s_mov_b32 m0, s47
	s_nop 0
	global_load_lds_dwordx4 v[182:183], off
	s_waitcnt vmcnt(6)
	s_barrier
	v_mfma_f32_16x16x32_f16 v[30:33], v[198:201], v[230:233], v[30:33]
	v_mfma_f32_16x16x32_f16 v[26:29], v[198:201], v[238:241], v[26:29]
	v_mfma_f32_16x16x32_f16 v[22:25], v[206:209], v[230:233], v[22:25]
	v_mfma_f32_16x16x32_f16 v[18:21], v[206:209], v[238:241], v[18:21]
	v_mfma_f32_16x16x32_f16 v[14:17], v[214:217], v[230:233], v[14:17]
	v_mfma_f32_16x16x32_f16 v[10:13], v[214:217], v[238:241], v[10:13]
	v_mfma_f32_16x16x32_f16 v[6:9], v[222:225], v[230:233], v[6:9]
	v_mfma_f32_16x16x32_f16 v[2:5], v[222:225], v[238:241], v[2:5]
	v_mfma_f32_16x16x32_f16 v[30:33], v[202:205], v[234:237], v[30:33]
	v_mfma_f32_16x16x32_f16 v[26:29], v[202:205], v[242:245], v[26:29]
	v_mfma_f32_16x16x32_f16 v[22:25], v[210:213], v[234:237], v[22:25]
	v_mfma_f32_16x16x32_f16 v[18:21], v[210:213], v[242:245], v[18:21]
	v_mfma_f32_16x16x32_f16 v[14:17], v[218:221], v[234:237], v[14:17]
	v_mfma_f32_16x16x32_f16 v[10:13], v[218:221], v[242:245], v[10:13]
	v_mfma_f32_16x16x32_f16 v[6:9], v[226:229], v[234:237], v[6:9]
	v_mfma_f32_16x16x32_f16 v[2:5], v[226:229], v[242:245], v[2:5]
	s_add_i32 s46, s46, 2
	s_add_u32 s44, s44, 0x100
	s_addc_u32 s45, s45, 0
	s_cmp_lt_u32 s46, 4
	s_barrier
	s_cbranch_scc1 .LBB8_41
	s_add_u32 s42, s42, 0x20380
	s_addc_u32 s43, s43, 0
	v_readfirstlane_b32 s44, v177
	v_lshl_add_u64 v[130:131], v[130:131], 1, s[42:43]
	s_mov_b32 m0, s44
	ds_read_b128 v[134:137], v171
	ds_read_b128 v[138:141], v173
	ds_read_b128 v[154:157], v174
	ds_read_b128 v[168:171], v175
	ds_read_b128 v[182:185], v176
	ds_read_b128 v[186:189], v176 offset:1024
	ds_read_b128 v[190:193], v176 offset:2048
	ds_read_b128 v[194:197], v176 offset:3072
	ds_read_b128 v[198:201], v176 offset:4096
	ds_read_b128 v[202:205], v176 offset:5120
	ds_read_b128 v[206:209], v176 offset:6144
	ds_read_b128 v[210:213], v176 offset:7168
	global_load_lds_dwordx4 v[130:131], off
	v_lshl_add_u64 v[130:131], v[132:133], 1, s[42:43]
	v_readfirstlane_b32 s42, v178
	s_mov_b32 m0, s42
	s_nop 0
	global_load_lds_dwordx4 v[130:131], off
	s_barrier
	s_waitcnt lgkmcnt(0)
	v_mfma_f32_16x16x32_f16 v[122:125], v[182:185], v[154:157], v[122:125]
	v_mfma_f32_16x16x32_f16 v[110:113], v[198:201], v[134:137], v[110:113]
	v_mfma_f32_16x16x32_f16 v[98:101], v[206:209], v[154:157], v[98:101]
	v_mfma_f32_16x16x32_f16 v[126:129], v[182:185], v[134:137], v[126:129]
	v_mfma_f32_16x16x32_f16 v[122:125], v[186:189], v[168:171], v[122:125]
	v_mfma_f32_16x16x32_f16 v[118:121], v[190:193], v[134:137], v[118:121]
	v_mfma_f32_16x16x32_f16 v[114:117], v[190:193], v[154:157], v[114:117]
	v_mfma_f32_16x16x32_f16 v[130:133], v[202:205], v[138:141], v[110:113]
	v_mfma_f32_16x16x32_f16 v[106:109], v[198:201], v[154:157], v[106:109]
	v_mfma_f32_16x16x32_f16 v[102:105], v[206:209], v[134:137], v[102:105]
	v_mfma_f32_16x16x32_f16 v[98:101], v[210:213], v[168:171], v[98:101]
	v_mfma_f32_16x16x32_f16 v[126:129], v[186:189], v[138:141], v[126:129]
	v_mfma_f32_16x16x32_f16 v[118:121], v[194:197], v[138:141], v[118:121]
	v_mfma_f32_16x16x32_f16 v[114:117], v[194:197], v[168:171], v[114:117]
	v_mfma_f32_16x16x32_f16 v[214:217], v[202:205], v[168:171], v[106:109]
	v_mfma_f32_16x16x32_f16 v[102:105], v[210:213], v[138:141], v[102:105]
	s_barrier
	ds_read_b128 v[106:109], v162
	ds_read_b128 v[110:113], v163
	ds_read_b128 v[160:163], v164
	ds_read_b128 v[218:221], v165
	s_barrier
	s_waitcnt lgkmcnt(0)
	v_mfma_f32_16x16x32_f16 v[82:85], v[190:193], v[160:163], v[82:85]
	v_mfma_f32_16x16x32_f16 v[78:81], v[198:201], v[106:109], v[78:81]
	v_mfma_f32_16x16x32_f16 v[74:77], v[198:201], v[160:163], v[74:77]
	v_mfma_f32_16x16x32_f16 v[70:73], v[206:209], v[106:109], v[70:73]
	v_mfma_f32_16x16x32_f16 v[66:69], v[206:209], v[160:163], v[66:69]
	v_mfma_f32_16x16x32_f16 v[94:97], v[182:185], v[106:109], v[94:97]
	v_mfma_f32_16x16x32_f16 v[90:93], v[182:185], v[160:163], v[90:93]
	v_mfma_f32_16x16x32_f16 v[86:89], v[190:193], v[106:109], v[86:89]
	v_mfma_f32_16x16x32_f16 v[82:85], v[194:197], v[218:221], v[82:85]
	v_mfma_f32_16x16x32_f16 v[78:81], v[202:205], v[110:113], v[78:81]
	v_mfma_f32_16x16x32_f16 v[74:77], v[202:205], v[218:221], v[74:77]
	v_mfma_f32_16x16x32_f16 v[70:73], v[210:213], v[110:113], v[70:73]
	v_mfma_f32_16x16x32_f16 v[66:69], v[210:213], v[218:221], v[66:69]
	v_mfma_f32_16x16x32_f16 v[222:225], v[186:189], v[110:113], v[94:97]
	v_mfma_f32_16x16x32_f16 v[182:185], v[186:189], v[218:221], v[90:93]
	v_mfma_f32_16x16x32_f16 v[86:89], v[194:197], v[110:113], v[86:89]
	s_barrier
	ds_read_b128 v[90:93], v176 offset:16384
	ds_read_b128 v[94:97], v176 offset:17408
	ds_read_b128 v[186:189], v176 offset:18432
	ds_read_b128 v[190:193], v176 offset:19456
	ds_read_b128 v[194:197], v176 offset:20480
	ds_read_b128 v[198:201], v176 offset:21504
	ds_read_b128 v[202:205], v176 offset:22528
	ds_read_b128 v[206:209], v176 offset:23552
	s_waitcnt vmcnt(4)
	s_barrier
	s_waitcnt lgkmcnt(0)
	v_mfma_f32_16x16x32_f16 v[46:49], v[194:197], v[134:137], v[46:49]
	v_mfma_f32_16x16x32_f16 v[42:45], v[194:197], v[154:157], v[42:45]
	v_mfma_f32_16x16x32_f16 v[38:41], v[202:205], v[134:137], v[38:41]
	v_mfma_f32_16x16x32_f16 v[34:37], v[202:205], v[154:157], v[34:37]
	v_mfma_f32_16x16x32_f16 v[62:65], v[90:93], v[134:137], v[62:65]
	v_mfma_f32_16x16x32_f16 v[58:61], v[90:93], v[154:157], v[58:61]
	v_mfma_f32_16x16x32_f16 v[54:57], v[186:189], v[134:137], v[54:57]
	v_mfma_f32_16x16x32_f16 v[50:53], v[186:189], v[154:157], v[50:53]
	v_mfma_f32_16x16x32_f16 v[46:49], v[198:201], v[138:141], v[46:49]
	v_mfma_f32_16x16x32_f16 v[42:45], v[198:201], v[168:171], v[42:45]
	v_mfma_f32_16x16x32_f16 v[38:41], v[206:209], v[138:141], v[38:41]
	v_mfma_f32_16x16x32_f16 v[34:37], v[206:209], v[168:171], v[34:37]
	v_mfma_f32_16x16x32_f16 v[210:213], v[94:97], v[138:141], v[62:65]
	v_mfma_f32_16x16x32_f16 v[226:229], v[94:97], v[168:171], v[58:61]
	v_mfma_f32_16x16x32_f16 v[230:233], v[190:193], v[138:141], v[54:57]
	v_mfma_f32_16x16x32_f16 v[234:237], v[190:193], v[168:171], v[50:53]
	v_mfma_f32_16x16x32_f16 v[2:5], v[202:205], v[160:163], v[2:5]
	v_mfma_f32_16x16x32_f16 v[30:33], v[90:93], v[106:109], v[30:33]
	v_mfma_f32_16x16x32_f16 v[26:29], v[90:93], v[160:163], v[26:29]
	v_mfma_f32_16x16x32_f16 v[22:25], v[186:189], v[106:109], v[22:25]
	v_mfma_f32_16x16x32_f16 v[18:21], v[186:189], v[160:163], v[18:21]
	v_mfma_f32_16x16x32_f16 v[14:17], v[194:197], v[106:109], v[14:17]
	v_mfma_f32_16x16x32_f16 v[10:13], v[194:197], v[160:163], v[10:13]
	v_mfma_f32_16x16x32_f16 v[6:9], v[202:205], v[106:109], v[6:9]
	v_mfma_f32_16x16x32_f16 v[2:5], v[206:209], v[218:221], v[2:5]
	v_mfma_f32_16x16x32_f16 v[138:141], v[94:97], v[110:113], v[30:33]
	v_mfma_f32_16x16x32_f16 v[168:171], v[94:97], v[218:221], v[26:29]
	v_mfma_f32_16x16x32_f16 v[238:241], v[190:193], v[110:113], v[22:25]
	v_mfma_f32_16x16x32_f16 v[186:189], v[190:193], v[218:221], v[18:21]
	v_mfma_f32_16x16x32_f16 v[190:193], v[198:201], v[110:113], v[14:17]
	v_mfma_f32_16x16x32_f16 v[194:197], v[198:201], v[218:221], v[10:13]
	v_mfma_f32_16x16x32_f16 v[198:201], v[206:209], v[110:113], v[6:9]
	s_barrier
	s_nop 0
	ds_read_b128 v[6:9], v144
	ds_read_b128 v[10:13], v145
	ds_read_b128 v[14:17], v146
	ds_read_b128 v[160:163], v147
	ds_read_b128 v[18:21], v176 offset:32768
	ds_read_b128 v[22:25], v176 offset:33792
	ds_read_b128 v[26:29], v176 offset:34816
	ds_read_b128 v[50:53], v176 offset:35840
	ds_read_b128 v[202:205], v176 offset:36864
	ds_read_b128 v[206:209], v176 offset:37888
	ds_read_b128 v[218:221], v176 offset:38912
	ds_read_b128 v[242:245], v176 offset:39936
	s_waitcnt vmcnt(2)
	s_barrier
	s_waitcnt lgkmcnt(0)
	v_mfma_f32_16x16x32_f16 v[30:33], v[18:21], v[6:9], v[126:129]
	v_mfma_f32_16x16x32_f16 v[154:157], v[22:25], v[10:13], v[30:33]
	v_mfma_f32_16x16x32_f16 v[30:33], v[18:21], v[14:17], v[122:125]
	v_mfma_f32_16x16x32_f16 v[110:113], v[22:25], v[160:163], v[30:33]
	v_mfma_f32_16x16x32_f16 v[30:33], v[26:29], v[6:9], v[118:121]
	v_mfma_f32_16x16x32_f16 v[146:149], v[50:53], v[10:13], v[30:33]
	v_mfma_f32_16x16x32_f16 v[30:33], v[26:29], v[14:17], v[114:117]
	v_mfma_f32_16x16x32_f16 v[106:109], v[50:53], v[160:163], v[30:33]
	v_mfma_f32_16x16x32_f16 v[30:33], v[202:205], v[6:9], v[130:133]
	v_mfma_f32_16x16x32_f16 v[142:145], v[206:209], v[10:13], v[30:33]
	v_mfma_f32_16x16x32_f16 v[30:33], v[202:205], v[14:17], v[214:217]
	v_mfma_f32_16x16x32_f16 v[94:97], v[206:209], v[160:163], v[30:33]
	v_mfma_f32_16x16x32_f16 v[30:33], v[218:221], v[6:9], v[102:105]
	v_mfma_f32_16x16x32_f16 v[134:137], v[242:245], v[10:13], v[30:33]
	v_mfma_f32_16x16x32_f16 v[30:33], v[218:221], v[14:17], v[98:101]
	v_mfma_f32_16x16x32_f16 v[90:93], v[242:245], v[160:163], v[30:33]
	s_barrier
	ds_read_b128 v[102:105], v150
	ds_read_b128 v[114:117], v151
	ds_read_b128 v[118:121], v152
	ds_read_b128 v[126:129], v153
	s_waitcnt vmcnt(0)
	s_barrier
	s_waitcnt lgkmcnt(0)
	v_mfma_f32_16x16x32_f16 v[30:33], v[18:21], v[102:105], v[222:225]
	v_mfma_f32_16x16x32_f16 v[18:21], v[18:21], v[118:121], v[182:185]
	v_mfma_f32_16x16x32_f16 v[62:65], v[22:25], v[114:117], v[30:33]
	v_mfma_f32_16x16x32_f16 v[30:33], v[22:25], v[126:129], v[18:21]
	v_mfma_f32_16x16x32_f16 v[18:21], v[26:29], v[102:105], v[86:89]
	v_mfma_f32_16x16x32_f16 v[58:61], v[50:53], v[114:117], v[18:21]
	v_mfma_f32_16x16x32_f16 v[18:21], v[26:29], v[118:121], v[82:85]
	v_mfma_f32_16x16x32_f16 v[26:29], v[50:53], v[126:129], v[18:21]
	v_mfma_f32_16x16x32_f16 v[18:21], v[202:205], v[102:105], v[78:81]
	v_mfma_f32_16x16x32_f16 v[54:57], v[206:209], v[114:117], v[18:21]
	v_mfma_f32_16x16x32_f16 v[18:21], v[202:205], v[118:121], v[74:77]
	v_mfma_f32_16x16x32_f16 v[22:25], v[206:209], v[126:129], v[18:21]
	v_mfma_f32_16x16x32_f16 v[18:21], v[218:221], v[102:105], v[70:73]
	v_mfma_f32_16x16x32_f16 v[50:53], v[242:245], v[114:117], v[18:21]
	v_mfma_f32_16x16x32_f16 v[18:21], v[218:221], v[118:121], v[66:69]
	v_mfma_f32_16x16x32_f16 v[18:21], v[242:245], v[126:129], v[18:21]
	s_barrier
	ds_read_b128 v[86:89], v176 offset:49152
	ds_read_b128 v[150:153], v176 offset:50176
	ds_read_b128 v[182:185], v176 offset:51200
	ds_read_b128 v[202:205], v176 offset:52224
	ds_read_b128 v[206:209], v176 offset:53248
	ds_read_b128 v[214:217], v176 offset:54272
	ds_read_b128 v[218:221], v176 offset:55296
	ds_read_b128 v[174:177], v176 offset:56320
	s_barrier
	s_waitcnt lgkmcnt(0)
	v_mfma_f32_16x16x32_f16 v[66:69], v[86:89], v[6:9], v[210:213]
	v_mfma_f32_16x16x32_f16 v[130:133], v[150:153], v[10:13], v[66:69]
	v_mfma_f32_16x16x32_f16 v[66:69], v[86:89], v[14:17], v[226:229]
	v_mfma_f32_16x16x32_f16 v[78:81], v[150:153], v[160:163], v[66:69]
	v_mfma_f32_16x16x32_f16 v[66:69], v[182:185], v[6:9], v[230:233]
	v_mfma_f32_16x16x32_f16 v[46:49], v[206:209], v[6:9], v[46:49]
	v_mfma_f32_16x16x32_f16 v[6:9], v[218:221], v[6:9], v[38:41]
	v_mfma_f32_16x16x32_f16 v[122:125], v[202:205], v[10:13], v[66:69]
	v_mfma_f32_16x16x32_f16 v[66:69], v[182:185], v[14:17], v[234:237]
	v_mfma_f32_16x16x32_f16 v[42:45], v[206:209], v[14:17], v[42:45]
	v_mfma_f32_16x16x32_f16 v[82:85], v[174:177], v[10:13], v[6:9]
	v_mfma_f32_16x16x32_f16 v[6:9], v[218:221], v[14:17], v[34:37]
	v_mfma_f32_16x16x32_f16 v[74:77], v[202:205], v[160:163], v[66:69]
	v_mfma_f32_16x16x32_f16 v[98:101], v[214:217], v[10:13], v[46:49]
	v_mfma_f32_16x16x32_f16 v[70:73], v[214:217], v[160:163], v[42:45]
	v_mfma_f32_16x16x32_f16 v[66:69], v[174:177], v[160:163], v[6:9]
	v_mfma_f32_16x16x32_f16 v[6:9], v[86:89], v[102:105], v[138:141]
	v_mfma_f32_16x16x32_f16 v[46:49], v[150:153], v[114:117], v[6:9]
	v_mfma_f32_16x16x32_f16 v[6:9], v[86:89], v[118:121], v[168:171]
	v_mfma_f32_16x16x32_f16 v[14:17], v[150:153], v[126:129], v[6:9]
	v_mfma_f32_16x16x32_f16 v[6:9], v[182:185], v[102:105], v[238:241]
	v_mfma_f32_16x16x32_f16 v[42:45], v[202:205], v[114:117], v[6:9]
	v_mfma_f32_16x16x32_f16 v[6:9], v[182:185], v[118:121], v[186:189]
	v_mfma_f32_16x16x32_f16 v[10:13], v[202:205], v[126:129], v[6:9]
	v_mfma_f32_16x16x32_f16 v[6:9], v[206:209], v[102:105], v[190:193]
	v_mfma_f32_16x16x32_f16 v[38:41], v[214:217], v[114:117], v[6:9]
	v_mfma_f32_16x16x32_f16 v[6:9], v[206:209], v[118:121], v[194:197]
	v_mfma_f32_16x16x32_f16 v[34:37], v[218:221], v[102:105], v[198:201]
	v_mfma_f32_16x16x32_f16 v[2:5], v[218:221], v[118:121], v[2:5]
	v_mfma_f32_16x16x32_f16 v[6:9], v[214:217], v[126:129], v[6:9]
	v_mfma_f32_16x16x32_f16 v[34:37], v[174:177], v[114:117], v[34:37]
	v_mfma_f32_16x16x32_f16 v[2:5], v[174:177], v[126:129], v[2:5]
	s_cmpk_gt_u32 s62, 0xff
	s_barrier
	s_cbranch_scc1 .LBB8_44
	s_barrier

.LBB9_38:
	ds_read_b128 v[176:179], v169
	ds_read_b128 v[180:183], v170
	ds_read_b128 v[184:187], v171
	ds_read_b128 v[188:191], v172
	v_add_u32_e32 v174, 0xc000, v152
	v_lshl_add_u64 v[192:193], v[136:137], 0, s[42:43]
	v_readfirstlane_b32 s45, v174
	v_add_u32_e32 v175, 0xe000, v152
	v_add_u32_e32 v173, s39, v168
	v_lshl_add_u64 v[230:231], v[192:193], 0, s[10:11]
	s_mov_b32 m0, s45
	v_lshl_add_u64 v[246:247], v[134:135], 0, s[42:43]
	v_readfirstlane_b32 s45, v175
	ds_read_b128 v[198:201], v173
	ds_read_b128 v[202:205], v173 offset:1024
	ds_read_b128 v[206:209], v173 offset:2048
	ds_read_b128 v[210:213], v173 offset:3072
	ds_read_b128 v[214:217], v173 offset:4096
	ds_read_b128 v[218:221], v173 offset:5120
	ds_read_b128 v[222:225], v173 offset:6144
	ds_read_b128 v[226:229], v173 offset:7168
	global_load_lds_dwordx4 v[230:231], off
	v_lshl_add_u64 v[230:231], v[246:247], 0, s[10:11]
	s_mov_b32 m0, s45
	s_nop 0
	global_load_lds_dwordx4 v[230:231], off
	s_waitcnt lgkmcnt(8)
	s_barrier
	s_waitcnt lgkmcnt(0)
	v_mfma_f32_16x16x32_f16 v[2:5], v[198:201], v[176:179], v[2:5]
	v_mfma_f32_16x16x32_f16 v[6:9], v[198:201], v[184:187], v[6:9]
	v_mfma_f32_16x16x32_f16 v[10:13], v[206:209], v[176:179], v[10:13]
	v_mfma_f32_16x16x32_f16 v[18:21], v[206:209], v[184:187], v[18:21]
	v_mfma_f32_16x16x32_f16 v[30:33], v[214:217], v[176:179], v[30:33]
	v_mfma_f32_16x16x32_f16 v[42:45], v[214:217], v[184:187], v[42:45]
	v_mfma_f32_16x16x32_f16 v[54:57], v[222:225], v[176:179], v[54:57]
	v_mfma_f32_16x16x32_f16 v[66:69], v[222:225], v[184:187], v[66:69]
	v_mfma_f32_16x16x32_f16 v[2:5], v[202:205], v[180:183], v[2:5]
	v_mfma_f32_16x16x32_f16 v[6:9], v[202:205], v[188:191], v[6:9]
	v_mfma_f32_16x16x32_f16 v[10:13], v[210:213], v[180:183], v[10:13]
	v_mfma_f32_16x16x32_f16 v[18:21], v[210:213], v[188:191], v[18:21]
	v_mfma_f32_16x16x32_f16 v[30:33], v[218:221], v[180:183], v[30:33]
	v_mfma_f32_16x16x32_f16 v[42:45], v[218:221], v[188:191], v[42:45]
	v_mfma_f32_16x16x32_f16 v[54:57], v[226:229], v[180:183], v[54:57]
	v_mfma_f32_16x16x32_f16 v[66:69], v[226:229], v[188:191], v[66:69]
	s_barrier
	v_lshl_add_u64 v[248:249], v[140:141], 0, s[42:43]
	v_readfirstlane_b32 s45, v142
	v_lshl_add_u64 v[250:251], v[248:249], 0, s[26:27]
	s_mov_b32 m0, s45
	ds_read_b128 v[230:233], v161
	ds_read_b128 v[234:237], v162
	ds_read_b128 v[238:241], v163
	ds_read_b128 v[242:245], v164
	global_load_lds_dwordx4 v[250:251], off
	v_lshl_add_u64 v[250:251], v[138:139], 0, s[42:43]
	v_readfirstlane_b32 s45, v143
	v_lshl_add_u64 v[252:253], v[250:251], 0, s[26:27]
	s_mov_b32 m0, s45
	s_nop 0
	global_load_lds_dwordx4 v[252:253], off
	s_barrier
	s_waitcnt lgkmcnt(0)
	v_mfma_f32_16x16x32_f16 v[14:17], v[198:201], v[230:233], v[14:17]
	v_mfma_f32_16x16x32_f16 v[22:25], v[198:201], v[238:241], v[22:25]
	v_mfma_f32_16x16x32_f16 v[34:37], v[206:209], v[230:233], v[34:37]
	v_mfma_f32_16x16x32_f16 v[46:49], v[206:209], v[238:241], v[46:49]
	v_mfma_f32_16x16x32_f16 v[58:61], v[214:217], v[230:233], v[58:61]
	v_mfma_f32_16x16x32_f16 v[70:73], v[214:217], v[238:241], v[70:73]
	v_mfma_f32_16x16x32_f16 v[78:81], v[222:225], v[230:233], v[78:81]
	v_mfma_f32_16x16x32_f16 v[86:89], v[222:225], v[238:241], v[86:89]
	v_mfma_f32_16x16x32_f16 v[14:17], v[202:205], v[234:237], v[14:17]
	v_mfma_f32_16x16x32_f16 v[22:25], v[202:205], v[242:245], v[22:25]
	v_mfma_f32_16x16x32_f16 v[34:37], v[210:213], v[234:237], v[34:37]
	v_mfma_f32_16x16x32_f16 v[46:49], v[210:213], v[242:245], v[46:49]
	v_mfma_f32_16x16x32_f16 v[58:61], v[218:221], v[234:237], v[58:61]
	v_mfma_f32_16x16x32_f16 v[70:73], v[218:221], v[242:245], v[70:73]
	v_mfma_f32_16x16x32_f16 v[78:81], v[226:229], v[234:237], v[78:81]
	v_mfma_f32_16x16x32_f16 v[86:89], v[226:229], v[242:245], v[86:89]
	v_readfirstlane_b32 s45, v152
	v_lshl_add_u64 v[252:253], v[192:193], 0, s[26:27]
	s_mov_b32 m0, s45
	v_readfirstlane_b32 s45, v153
	s_barrier
	ds_read_b128 v[198:201], v173 offset:16384
	ds_read_b128 v[202:205], v173 offset:17408
	ds_read_b128 v[206:209], v173 offset:18432
	ds_read_b128 v[210:213], v173 offset:19456
	ds_read_b128 v[214:217], v173 offset:20480
	ds_read_b128 v[218:221], v173 offset:21504
	ds_read_b128 v[222:225], v173 offset:22528
	ds_read_b128 v[226:229], v173 offset:23552
	global_load_lds_dwordx4 v[252:253], off
	v_lshl_add_u64 v[252:253], v[246:247], 0, s[26:27]
	s_mov_b32 m0, s45
	s_nop 0
	global_load_lds_dwordx4 v[252:253], off
	s_barrier
	s_waitcnt lgkmcnt(0)
	v_mfma_f32_16x16x32_f16 v[26:29], v[198:201], v[176:179], v[26:29]
	v_mfma_f32_16x16x32_f16 v[38:41], v[198:201], v[184:187], v[38:41]
	v_mfma_f32_16x16x32_f16 v[50:53], v[206:209], v[176:179], v[50:53]
	v_mfma_f32_16x16x32_f16 v[62:65], v[206:209], v[184:187], v[62:65]
	v_mfma_f32_16x16x32_f16 v[74:77], v[214:217], v[176:179], v[74:77]
	v_mfma_f32_16x16x32_f16 v[82:85], v[214:217], v[184:187], v[82:85]
	v_mfma_f32_16x16x32_f16 v[90:93], v[222:225], v[176:179], v[90:93]
	v_mfma_f32_16x16x32_f16 v[94:97], v[222:225], v[184:187], v[94:97]
	v_mfma_f32_16x16x32_f16 v[26:29], v[202:205], v[180:183], v[26:29]
	v_mfma_f32_16x16x32_f16 v[38:41], v[202:205], v[188:191], v[38:41]
	v_mfma_f32_16x16x32_f16 v[50:53], v[210:213], v[180:183], v[50:53]
	v_mfma_f32_16x16x32_f16 v[62:65], v[210:213], v[188:191], v[62:65]
	v_mfma_f32_16x16x32_f16 v[74:77], v[218:221], v[180:183], v[74:77]
	v_mfma_f32_16x16x32_f16 v[82:85], v[218:221], v[188:191], v[82:85]
	v_mfma_f32_16x16x32_f16 v[90:93], v[226:229], v[180:183], v[90:93]
	v_mfma_f32_16x16x32_f16 v[94:97], v[226:229], v[188:191], v[94:97]
	s_barrier
	v_readfirstlane_b32 s45, v154
	v_lshl_add_u64 v[176:177], v[248:249], 0, s[28:29]
	s_mov_b32 m0, s45
	v_readfirstlane_b32 s45, v155
	global_load_lds_dwordx4 v[176:177], off
	v_lshl_add_u64 v[176:177], v[250:251], 0, s[28:29]
	s_mov_b32 m0, s45
	s_nop 0
	global_load_lds_dwordx4 v[176:177], off
	s_waitcnt vmcnt(6)
	s_barrier
	v_mfma_f32_16x16x32_f16 v[98:101], v[198:201], v[230:233], v[98:101]
	v_mfma_f32_16x16x32_f16 v[102:105], v[198:201], v[238:241], v[102:105]
	v_mfma_f32_16x16x32_f16 v[106:109], v[206:209], v[230:233], v[106:109]
	v_mfma_f32_16x16x32_f16 v[110:113], v[206:209], v[238:241], v[110:113]
	v_mfma_f32_16x16x32_f16 v[114:117], v[214:217], v[230:233], v[114:117]
	v_mfma_f32_16x16x32_f16 v[118:121], v[214:217], v[238:241], v[118:121]
	v_mfma_f32_16x16x32_f16 v[122:125], v[222:225], v[230:233], v[122:125]
	v_mfma_f32_16x16x32_f16 v[126:129], v[222:225], v[238:241], v[126:129]
	v_mfma_f32_16x16x32_f16 v[98:101], v[202:205], v[234:237], v[98:101]
	v_mfma_f32_16x16x32_f16 v[102:105], v[202:205], v[242:245], v[102:105]
	v_mfma_f32_16x16x32_f16 v[106:109], v[210:213], v[234:237], v[106:109]
	v_mfma_f32_16x16x32_f16 v[110:113], v[210:213], v[242:245], v[110:113]
	v_mfma_f32_16x16x32_f16 v[114:117], v[218:221], v[234:237], v[114:117]
	v_mfma_f32_16x16x32_f16 v[118:121], v[218:221], v[242:245], v[118:121]
	v_mfma_f32_16x16x32_f16 v[122:125], v[226:229], v[234:237], v[122:125]
	v_mfma_f32_16x16x32_f16 v[126:129], v[226:229], v[242:245], v[126:129]
	s_barrier
	ds_read_b128 v[176:179], v144
	ds_read_b128 v[180:183], v145
	ds_read_b128 v[184:187], v150
	ds_read_b128 v[188:191], v151
	v_readfirstlane_b32 s45, v156
	v_lshl_add_u64 v[230:231], v[192:193], 0, s[28:29]
	s_mov_b32 m0, s45
	v_readfirstlane_b32 s45, v157
	ds_read_b128 v[198:201], v173 offset:32768
	ds_read_b128 v[202:205], v173 offset:33792
	ds_read_b128 v[206:209], v173 offset:34816
	ds_read_b128 v[210:213], v173 offset:35840
	ds_read_b128 v[214:217], v173 offset:36864
	ds_read_b128 v[218:221], v173 offset:37888
	ds_read_b128 v[222:225], v173 offset:38912
	ds_read_b128 v[226:229], v173 offset:39936
	global_load_lds_dwordx4 v[230:231], off
	v_lshl_add_u64 v[230:231], v[246:247], 0, s[28:29]
	s_mov_b32 m0, s45
	s_nop 0
	global_load_lds_dwordx4 v[230:231], off
	s_waitcnt lgkmcnt(8)
	s_barrier
	s_waitcnt lgkmcnt(0)
	v_mfma_f32_16x16x32_f16 v[2:5], v[198:201], v[176:179], v[2:5]
	v_mfma_f32_16x16x32_f16 v[6:9], v[198:201], v[184:187], v[6:9]
	v_mfma_f32_16x16x32_f16 v[10:13], v[206:209], v[176:179], v[10:13]
	v_mfma_f32_16x16x32_f16 v[18:21], v[206:209], v[184:187], v[18:21]
	v_mfma_f32_16x16x32_f16 v[30:33], v[214:217], v[176:179], v[30:33]
	v_mfma_f32_16x16x32_f16 v[42:45], v[214:217], v[184:187], v[42:45]
	v_mfma_f32_16x16x32_f16 v[54:57], v[222:225], v[176:179], v[54:57]
	v_mfma_f32_16x16x32_f16 v[66:69], v[222:225], v[184:187], v[66:69]
	v_mfma_f32_16x16x32_f16 v[2:5], v[202:205], v[180:183], v[2:5]
	v_mfma_f32_16x16x32_f16 v[6:9], v[202:205], v[188:191], v[6:9]
	v_mfma_f32_16x16x32_f16 v[10:13], v[210:213], v[180:183], v[10:13]
	v_mfma_f32_16x16x32_f16 v[18:21], v[210:213], v[188:191], v[18:21]
	v_mfma_f32_16x16x32_f16 v[30:33], v[218:221], v[180:183], v[30:33]
	v_mfma_f32_16x16x32_f16 v[42:45], v[218:221], v[188:191], v[42:45]
	v_mfma_f32_16x16x32_f16 v[54:57], v[226:229], v[180:183], v[54:57]
	v_mfma_f32_16x16x32_f16 v[66:69], v[226:229], v[188:191], v[66:69]
	s_barrier
	v_readfirstlane_b32 s45, v158
	v_lshl_add_u64 v[252:253], v[248:249], 0, s[30:31]
	s_mov_b32 m0, s45
	v_readfirstlane_b32 s45, v159
	ds_read_b128 v[230:233], v146
	ds_read_b128 v[234:237], v147
	ds_read_b128 v[238:241], v148
	ds_read_b128 v[242:245], v149
	global_load_lds_dwordx4 v[252:253], off
	v_lshl_add_u64 v[252:253], v[250:251], 0, s[30:31]
	s_mov_b32 m0, s45
	s_nop 0
	global_load_lds_dwordx4 v[252:253], off
	s_barrier
	s_waitcnt lgkmcnt(0)
	v_mfma_f32_16x16x32_f16 v[14:17], v[198:201], v[230:233], v[14:17]
	v_mfma_f32_16x16x32_f16 v[22:25], v[198:201], v[238:241], v[22:25]
	v_mfma_f32_16x16x32_f16 v[34:37], v[206:209], v[230:233], v[34:37]
	v_mfma_f32_16x16x32_f16 v[46:49], v[206:209], v[238:241], v[46:49]
	v_mfma_f32_16x16x32_f16 v[58:61], v[214:217], v[230:233], v[58:61]
	v_mfma_f32_16x16x32_f16 v[70:73], v[214:217], v[238:241], v[70:73]
	v_mfma_f32_16x16x32_f16 v[78:81], v[222:225], v[230:233], v[78:81]
	v_mfma_f32_16x16x32_f16 v[86:89], v[222:225], v[238:241], v[86:89]
	v_mfma_f32_16x16x32_f16 v[14:17], v[202:205], v[234:237], v[14:17]
	v_mfma_f32_16x16x32_f16 v[22:25], v[202:205], v[242:245], v[22:25]
	v_mfma_f32_16x16x32_f16 v[34:37], v[210:213], v[234:237], v[34:37]
	v_mfma_f32_16x16x32_f16 v[46:49], v[210:213], v[242:245], v[46:49]
	v_mfma_f32_16x16x32_f16 v[58:61], v[218:221], v[234:237], v[58:61]
	v_mfma_f32_16x16x32_f16 v[70:73], v[218:221], v[242:245], v[70:73]
	v_mfma_f32_16x16x32_f16 v[78:81], v[226:229], v[234:237], v[78:81]
	v_mfma_f32_16x16x32_f16 v[86:89], v[226:229], v[242:245], v[86:89]
	v_readfirstlane_b32 s45, v160
	v_lshl_add_u64 v[192:193], v[192:193], 0, s[30:31]
	s_mov_b32 m0, s45
	v_readfirstlane_b32 s45, v165
	s_barrier
	ds_read_b128 v[198:201], v173 offset:49152
	ds_read_b128 v[202:205], v173 offset:50176
	ds_read_b128 v[206:209], v173 offset:51200
	ds_read_b128 v[210:213], v173 offset:52224
	ds_read_b128 v[214:217], v173 offset:53248
	ds_read_b128 v[218:221], v173 offset:54272
	ds_read_b128 v[222:225], v173 offset:55296
	ds_read_b128 v[226:229], v173 offset:56320
	global_load_lds_dwordx4 v[192:193], off
	v_lshl_add_u64 v[192:193], v[246:247], 0, s[30:31]
	s_mov_b32 m0, s45
	s_nop 0
	global_load_lds_dwordx4 v[192:193], off
	s_barrier
	s_waitcnt lgkmcnt(0)
	v_mfma_f32_16x16x32_f16 v[26:29], v[198:201], v[176:179], v[26:29]
	v_mfma_f32_16x16x32_f16 v[38:41], v[198:201], v[184:187], v[38:41]
	v_mfma_f32_16x16x32_f16 v[50:53], v[206:209], v[176:179], v[50:53]
	v_mfma_f32_16x16x32_f16 v[62:65], v[206:209], v[184:187], v[62:65]
	v_mfma_f32_16x16x32_f16 v[74:77], v[214:217], v[176:179], v[74:77]
	v_mfma_f32_16x16x32_f16 v[82:85], v[214:217], v[184:187], v[82:85]
	v_mfma_f32_16x16x32_f16 v[90:93], v[222:225], v[176:179], v[90:93]
	v_mfma_f32_16x16x32_f16 v[94:97], v[222:225], v[184:187], v[94:97]
	v_mfma_f32_16x16x32_f16 v[26:29], v[202:205], v[180:183], v[26:29]
	v_mfma_f32_16x16x32_f16 v[38:41], v[202:205], v[188:191], v[38:41]
	v_mfma_f32_16x16x32_f16 v[50:53], v[210:213], v[180:183], v[50:53]
	v_mfma_f32_16x16x32_f16 v[62:65], v[210:213], v[188:191], v[62:65]
	v_mfma_f32_16x16x32_f16 v[74:77], v[218:221], v[180:183], v[74:77]
	v_mfma_f32_16x16x32_f16 v[82:85], v[218:221], v[188:191], v[82:85]
	v_mfma_f32_16x16x32_f16 v[90:93], v[226:229], v[180:183], v[90:93]
	v_mfma_f32_16x16x32_f16 v[94:97], v[226:229], v[188:191], v[94:97]
	s_barrier
	v_readfirstlane_b32 s45, v166
	v_lshl_add_u64 v[176:177], v[248:249], 0, s[34:35]
	s_mov_b32 m0, s45
	v_readfirstlane_b32 s45, v167
	global_load_lds_dwordx4 v[176:177], off
	v_lshl_add_u64 v[176:177], v[250:251], 0, s[34:35]
	s_mov_b32 m0, s45
	s_nop 0
	global_load_lds_dwordx4 v[176:177], off
	s_waitcnt vmcnt(6)
	s_barrier
	v_mfma_f32_16x16x32_f16 v[98:101], v[198:201], v[230:233], v[98:101]
	v_mfma_f32_16x16x32_f16 v[102:105], v[198:201], v[238:241], v[102:105]
	v_mfma_f32_16x16x32_f16 v[106:109], v[206:209], v[230:233], v[106:109]
	v_mfma_f32_16x16x32_f16 v[110:113], v[206:209], v[238:241], v[110:113]
	v_mfma_f32_16x16x32_f16 v[114:117], v[214:217], v[230:233], v[114:117]
	v_mfma_f32_16x16x32_f16 v[118:121], v[214:217], v[238:241], v[118:121]
	v_mfma_f32_16x16x32_f16 v[122:125], v[222:225], v[230:233], v[122:125]
	v_mfma_f32_16x16x32_f16 v[126:129], v[222:225], v[238:241], v[126:129]
	v_mfma_f32_16x16x32_f16 v[98:101], v[202:205], v[234:237], v[98:101]
	v_mfma_f32_16x16x32_f16 v[102:105], v[202:205], v[242:245], v[102:105]
	v_mfma_f32_16x16x32_f16 v[106:109], v[210:213], v[234:237], v[106:109]
	v_mfma_f32_16x16x32_f16 v[110:113], v[210:213], v[242:245], v[110:113]
	v_mfma_f32_16x16x32_f16 v[114:117], v[218:221], v[234:237], v[114:117]
	v_mfma_f32_16x16x32_f16 v[118:121], v[218:221], v[242:245], v[118:121]
	v_mfma_f32_16x16x32_f16 v[122:125], v[226:229], v[234:237], v[122:125]
	v_mfma_f32_16x16x32_f16 v[126:129], v[226:229], v[242:245], v[126:129]
	s_add_i32 s44, s44, 2
	s_add_u32 s42, s42, 0x100
	s_addc_u32 s43, s43, 0
	s_cmp_lt_u32 s44, 4
	s_barrier
	s_cbranch_scc1 .LBB9_38
	s_add_u32 s40, s40, 0x20380
	s_addc_u32 s41, s41, 0
	v_readfirstlane_b32 s39, v174
	v_lshl_add_u64 v[130:131], v[130:131], 1, s[40:41]
	s_mov_b32 m0, s39
	v_readfirstlane_b32 s39, v175
	ds_read_b128 v[134:137], v169
	ds_read_b128 v[138:141], v170
	ds_read_b128 v[152:155], v171
	ds_read_b128 v[156:159], v172
	ds_read_b128 v[166:169], v173
	ds_read_b128 v[176:179], v173 offset:1024
	ds_read_b128 v[180:183], v173 offset:2048
	ds_read_b128 v[184:187], v173 offset:3072
	ds_read_b128 v[188:191], v173 offset:4096
	ds_read_b128 v[198:201], v173 offset:5120
	ds_read_b128 v[202:205], v173 offset:6144
	ds_read_b128 v[206:209], v173 offset:7168
	global_load_lds_dwordx4 v[130:131], off
	v_lshl_add_u64 v[130:131], v[132:133], 1, s[40:41]
	s_mov_b32 m0, s39
	s_nop 0
	global_load_lds_dwordx4 v[130:131], off
	s_barrier
	s_waitcnt lgkmcnt(0)
	v_mfma_f32_16x16x32_f16 v[2:5], v[166:169], v[134:137], v[2:5]
	v_mfma_f32_16x16x32_f16 v[6:9], v[166:169], v[152:155], v[6:9]
	v_mfma_f32_16x16x32_f16 v[30:33], v[188:191], v[134:137], v[30:33]
	v_mfma_f32_16x16x32_f16 v[2:5], v[176:179], v[138:141], v[2:5]
	v_mfma_f32_16x16x32_f16 v[6:9], v[176:179], v[156:159], v[6:9]
	v_mfma_f32_16x16x32_f16 v[10:13], v[180:183], v[134:137], v[10:13]
	v_mfma_f32_16x16x32_f16 v[18:21], v[180:183], v[152:155], v[18:21]
	v_mfma_f32_16x16x32_f16 v[30:33], v[198:201], v[138:141], v[30:33]
	v_mfma_f32_16x16x32_f16 v[42:45], v[188:191], v[152:155], v[42:45]
	v_mfma_f32_16x16x32_f16 v[54:57], v[202:205], v[134:137], v[54:57]
	v_mfma_f32_16x16x32_f16 v[66:69], v[202:205], v[152:155], v[66:69]
	v_mfma_f32_16x16x32_f16 v[10:13], v[184:187], v[138:141], v[10:13]
	v_mfma_f32_16x16x32_f16 v[18:21], v[184:187], v[156:159], v[18:21]
	v_mfma_f32_16x16x32_f16 v[42:45], v[198:201], v[156:159], v[42:45]
	v_mfma_f32_16x16x32_f16 v[54:57], v[206:209], v[138:141], v[54:57]
	v_mfma_f32_16x16x32_f16 v[66:69], v[206:209], v[156:159], v[66:69]
	s_barrier
	ds_read_b128 v[130:133], v161
	ds_read_b128 v[210:213], v162
	ds_read_b128 v[160:163], v163
	ds_read_b128 v[214:217], v164
	s_barrier
	s_waitcnt lgkmcnt(0)
	v_mfma_f32_16x16x32_f16 v[58:61], v[188:191], v[130:133], v[58:61]
	v_mfma_f32_16x16x32_f16 v[14:17], v[166:169], v[130:133], v[14:17]
	v_mfma_f32_16x16x32_f16 v[22:25], v[166:169], v[160:163], v[22:25]
	v_mfma_f32_16x16x32_f16 v[164:167], v[198:201], v[210:213], v[58:61]
	v_mfma_f32_16x16x32_f16 v[58:61], v[188:191], v[160:163], v[70:73]
	v_mfma_f32_16x16x32_f16 v[46:49], v[180:183], v[160:163], v[46:49]
	v_mfma_f32_16x16x32_f16 v[168:171], v[198:201], v[214:217], v[58:61]
	v_mfma_f32_16x16x32_f16 v[58:61], v[202:205], v[130:133], v[78:81]
	v_mfma_f32_16x16x32_f16 v[14:17], v[176:179], v[210:213], v[14:17]
	v_mfma_f32_16x16x32_f16 v[34:37], v[180:183], v[130:133], v[34:37]
	v_mfma_f32_16x16x32_f16 v[46:49], v[184:187], v[214:217], v[46:49]
	v_mfma_f32_16x16x32_f16 v[78:81], v[206:209], v[210:213], v[58:61]
	v_mfma_f32_16x16x32_f16 v[58:61], v[202:205], v[160:163], v[86:89]
	v_mfma_f32_16x16x32_f16 v[22:25], v[176:179], v[214:217], v[22:25]
	v_mfma_f32_16x16x32_f16 v[34:37], v[184:187], v[210:213], v[34:37]
	v_mfma_f32_16x16x32_f16 v[86:89], v[206:209], v[214:217], v[58:61]
	s_barrier
	s_nop 2
	ds_read_b128 v[58:61], v173 offset:16384
	ds_read_b128 v[70:73], v173 offset:17408
	ds_read_b128 v[174:177], v173 offset:18432
	ds_read_b128 v[178:181], v173 offset:19456
	ds_read_b128 v[182:185], v173 offset:20480
	ds_read_b128 v[186:189], v173 offset:21504
	ds_read_b128 v[190:193], v173 offset:22528
	ds_read_b128 v[198:201], v173 offset:23552
	s_waitcnt vmcnt(4)
	s_barrier
	s_waitcnt lgkmcnt(0)
	v_mfma_f32_16x16x32_f16 v[26:29], v[58:61], v[134:137], v[26:29]
	v_mfma_f32_16x16x32_f16 v[26:29], v[70:73], v[138:141], v[26:29]
	v_mfma_f32_16x16x32_f16 v[38:41], v[58:61], v[152:155], v[38:41]
	v_mfma_f32_16x16x32_f16 v[50:53], v[174:177], v[134:137], v[50:53]
	v_mfma_f32_16x16x32_f16 v[62:65], v[174:177], v[152:155], v[62:65]
	v_mfma_f32_16x16x32_f16 v[74:77], v[182:185], v[134:137], v[74:77]
	v_mfma_f32_16x16x32_f16 v[82:85], v[182:185], v[152:155], v[82:85]
	v_mfma_f32_16x16x32_f16 v[90:93], v[190:193], v[134:137], v[90:93]
	v_mfma_f32_16x16x32_f16 v[94:97], v[190:193], v[152:155], v[94:97]
	v_mfma_f32_16x16x32_f16 v[38:41], v[70:73], v[156:159], v[38:41]
	v_mfma_f32_16x16x32_f16 v[50:53], v[178:181], v[138:141], v[50:53]
	v_mfma_f32_16x16x32_f16 v[62:65], v[178:181], v[156:159], v[62:65]
	v_mfma_f32_16x16x32_f16 v[74:77], v[186:189], v[138:141], v[74:77]
	v_mfma_f32_16x16x32_f16 v[82:85], v[186:189], v[156:159], v[82:85]
	v_mfma_f32_16x16x32_f16 v[90:93], v[198:201], v[138:141], v[90:93]
	v_mfma_f32_16x16x32_f16 v[94:97], v[198:201], v[156:159], v[94:97]
	v_mfma_f32_16x16x32_f16 v[98:101], v[58:61], v[130:133], v[98:101]
	v_mfma_f32_16x16x32_f16 v[58:61], v[58:61], v[160:163], v[102:105]
	v_mfma_f32_16x16x32_f16 v[102:105], v[70:73], v[214:217], v[58:61]
	v_mfma_f32_16x16x32_f16 v[58:61], v[174:177], v[130:133], v[106:109]
	v_mfma_f32_16x16x32_f16 v[106:109], v[178:181], v[210:213], v[58:61]
	v_mfma_f32_16x16x32_f16 v[58:61], v[174:177], v[160:163], v[110:113]
	v_mfma_f32_16x16x32_f16 v[202:205], v[178:181], v[214:217], v[58:61]
	v_mfma_f32_16x16x32_f16 v[58:61], v[182:185], v[130:133], v[114:117]
	v_mfma_f32_16x16x32_f16 v[206:209], v[186:189], v[210:213], v[58:61]
	v_mfma_f32_16x16x32_f16 v[58:61], v[182:185], v[160:163], v[118:121]
	v_mfma_f32_16x16x32_f16 v[218:221], v[186:189], v[214:217], v[58:61]
	v_mfma_f32_16x16x32_f16 v[58:61], v[190:193], v[130:133], v[122:125]
	v_mfma_f32_16x16x32_f16 v[98:101], v[70:73], v[210:213], v[98:101]
	v_mfma_f32_16x16x32_f16 v[210:213], v[198:201], v[210:213], v[58:61]
	v_mfma_f32_16x16x32_f16 v[58:61], v[190:193], v[160:163], v[126:129]
	v_mfma_f32_16x16x32_f16 v[198:201], v[198:201], v[214:217], v[58:61]
	s_barrier
	ds_read_b128 v[110:113], v144
	ds_read_b128 v[130:133], v145
	ds_read_b128 v[214:217], v150
	ds_read_b128 v[222:225], v151
	s_nop 0
	ds_read_b128 v[58:61], v173 offset:32768
	ds_read_b128 v[70:73], v173 offset:33792
	ds_read_b128 v[114:117], v173 offset:34816
	ds_read_b128 v[118:121], v173 offset:35840
	ds_read_b128 v[134:137], v173 offset:36864
	ds_read_b128 v[138:141], v173 offset:37888
	ds_read_b128 v[178:181], v173 offset:38912
	ds_read_b128 v[226:229], v173 offset:39936
	s_waitcnt vmcnt(2)
	s_barrier
	s_waitcnt lgkmcnt(0)
	v_mfma_f32_16x16x32_f16 v[2:5], v[58:61], v[110:113], v[2:5]
	v_mfma_f32_16x16x32_f16 v[190:193], v[70:73], v[130:133], v[2:5]
	v_mfma_f32_16x16x32_f16 v[2:5], v[58:61], v[214:217], v[6:9]
	v_mfma_f32_16x16x32_f16 v[158:161], v[70:73], v[222:225], v[2:5]
	v_mfma_f32_16x16x32_f16 v[2:5], v[114:117], v[110:113], v[10:13]
	v_mfma_f32_16x16x32_f16 v[186:189], v[118:121], v[130:133], v[2:5]
	v_mfma_f32_16x16x32_f16 v[2:5], v[114:117], v[214:217], v[18:21]
	v_mfma_f32_16x16x32_f16 v[154:157], v[118:121], v[222:225], v[2:5]
	v_mfma_f32_16x16x32_f16 v[2:5], v[134:137], v[110:113], v[30:33]
	v_mfma_f32_16x16x32_f16 v[182:185], v[138:141], v[130:133], v[2:5]
	v_mfma_f32_16x16x32_f16 v[2:5], v[134:137], v[214:217], v[42:45]
	v_mfma_f32_16x16x32_f16 v[150:153], v[138:141], v[222:225], v[2:5]
	v_mfma_f32_16x16x32_f16 v[2:5], v[178:181], v[110:113], v[54:57]
	v_mfma_f32_16x16x32_f16 v[174:177], v[226:229], v[130:133], v[2:5]
	v_mfma_f32_16x16x32_f16 v[2:5], v[178:181], v[214:217], v[66:69]
	v_mfma_f32_16x16x32_f16 v[142:145], v[226:229], v[222:225], v[2:5]
	s_barrier
	s_nop 4
	ds_read_b128 v[2:5], v146
	ds_read_b128 v[10:13], v147
	ds_read_b128 v[18:21], v148
	ds_read_b128 v[42:45], v149
	s_waitcnt vmcnt(0)
	s_barrier
	s_waitcnt lgkmcnt(0)
	v_mfma_f32_16x16x32_f16 v[6:9], v[58:61], v[2:5], v[14:17]
	v_mfma_f32_16x16x32_f16 v[126:129], v[70:73], v[10:13], v[6:9]
	v_mfma_f32_16x16x32_f16 v[6:9], v[58:61], v[18:21], v[22:25]
	v_mfma_f32_16x16x32_f16 v[70:73], v[70:73], v[42:45], v[6:9]
	v_mfma_f32_16x16x32_f16 v[6:9], v[114:117], v[2:5], v[34:37]
	v_mfma_f32_16x16x32_f16 v[122:125], v[118:121], v[10:13], v[6:9]
	v_mfma_f32_16x16x32_f16 v[6:9], v[114:117], v[18:21], v[46:49]
	v_mfma_f32_16x16x32_f16 v[58:61], v[118:121], v[42:45], v[6:9]
	v_mfma_f32_16x16x32_f16 v[6:9], v[134:137], v[2:5], v[164:167]
	v_mfma_f32_16x16x32_f16 v[118:121], v[138:141], v[10:13], v[6:9]
	v_mfma_f32_16x16x32_f16 v[6:9], v[134:137], v[18:21], v[168:171]
	v_mfma_f32_16x16x32_f16 v[46:49], v[138:141], v[42:45], v[6:9]
	v_mfma_f32_16x16x32_f16 v[6:9], v[178:181], v[2:5], v[78:81]
	v_mfma_f32_16x16x32_f16 v[114:117], v[226:229], v[10:13], v[6:9]
	v_mfma_f32_16x16x32_f16 v[6:9], v[178:181], v[18:21], v[86:89]
	v_mfma_f32_16x16x32_f16 v[30:33], v[226:229], v[42:45], v[6:9]
	s_barrier
	s_nop 4
	ds_read_b128 v[6:9], v173 offset:49152
	ds_read_b128 v[14:17], v173 offset:50176
	ds_read_b128 v[22:25], v173 offset:51200
	ds_read_b128 v[34:37], v173 offset:52224
	ds_read_b128 v[54:57], v173 offset:53248
	ds_read_b128 v[66:69], v173 offset:54272
	ds_read_b128 v[78:81], v173 offset:55296
	ds_read_b128 v[86:89], v173 offset:56320
	s_barrier
	s_waitcnt lgkmcnt(0)
	v_mfma_f32_16x16x32_f16 v[26:29], v[6:9], v[110:113], v[26:29]
	v_mfma_f32_16x16x32_f16 v[178:181], v[14:17], v[130:133], v[26:29]
	v_mfma_f32_16x16x32_f16 v[26:29], v[6:9], v[214:217], v[38:41]
	v_mfma_f32_16x16x32_f16 v[146:149], v[14:17], v[222:225], v[26:29]
	v_mfma_f32_16x16x32_f16 v[26:29], v[22:25], v[110:113], v[50:53]
	v_mfma_f32_16x16x32_f16 v[170:173], v[34:37], v[130:133], v[26:29]
	v_mfma_f32_16x16x32_f16 v[26:29], v[22:25], v[214:217], v[62:65]
	v_mfma_f32_16x16x32_f16 v[138:141], v[34:37], v[222:225], v[26:29]
	v_mfma_f32_16x16x32_f16 v[26:29], v[54:57], v[110:113], v[74:77]
	v_mfma_f32_16x16x32_f16 v[166:169], v[66:69], v[130:133], v[26:29]
	v_mfma_f32_16x16x32_f16 v[26:29], v[54:57], v[214:217], v[82:85]
	v_mfma_f32_16x16x32_f16 v[134:137], v[66:69], v[222:225], v[26:29]
	v_mfma_f32_16x16x32_f16 v[26:29], v[78:81], v[110:113], v[90:93]
	v_mfma_f32_16x16x32_f16 v[162:165], v[86:89], v[130:133], v[26:29]
	v_mfma_f32_16x16x32_f16 v[26:29], v[78:81], v[214:217], v[94:97]
	v_mfma_f32_16x16x32_f16 v[130:133], v[86:89], v[222:225], v[26:29]
	v_mfma_f32_16x16x32_f16 v[26:29], v[6:9], v[2:5], v[98:101]
	v_mfma_f32_16x16x32_f16 v[6:9], v[6:9], v[18:21], v[102:105]
	v_mfma_f32_16x16x32_f16 v[110:113], v[14:17], v[10:13], v[26:29]
	v_mfma_f32_16x16x32_f16 v[26:29], v[14:17], v[42:45], v[6:9]
	v_mfma_f32_16x16x32_f16 v[6:9], v[22:25], v[2:5], v[106:109]
	v_mfma_f32_16x16x32_f16 v[106:109], v[34:37], v[10:13], v[6:9]
	v_mfma_f32_16x16x32_f16 v[6:9], v[22:25], v[18:21], v[202:205]
	v_mfma_f32_16x16x32_f16 v[14:17], v[34:37], v[42:45], v[6:9]
	v_mfma_f32_16x16x32_f16 v[6:9], v[54:57], v[2:5], v[206:209]
	v_mfma_f32_16x16x32_f16 v[2:5], v[78:81], v[2:5], v[210:213]
	v_mfma_f32_16x16x32_f16 v[102:105], v[66:69], v[10:13], v[6:9]
	v_mfma_f32_16x16x32_f16 v[6:9], v[54:57], v[18:21], v[218:221]
	v_mfma_f32_16x16x32_f16 v[98:101], v[86:89], v[10:13], v[2:5]
	v_mfma_f32_16x16x32_f16 v[2:5], v[78:81], v[18:21], v[198:201]
	v_mfma_f32_16x16x32_f16 v[6:9], v[66:69], v[42:45], v[6:9]
	v_mfma_f32_16x16x32_f16 v[2:5], v[86:89], v[42:45], v[2:5]
	s_cmpk_gt_u32 s54, 0xff
	s_barrier
	s_cbranch_scc1 .LBB9_34
	s_barrier
	s_branch .LBB9_34

.LBB10_12:
	ds_read_b128 v[182:185], v171
	ds_read_b128 v[186:189], v173
	ds_read_b128 v[190:193], v174
	ds_read_b128 v[194:197], v175
	v_add_u32_e32 v177, 0xc000, v148
	v_lshl_add_u64 v[246:247], v[136:137], 0, s[44:45]
	v_readfirstlane_b32 s47, v177
	v_add_u32_e32 v176, s63, v170
	v_lshl_add_u64 v[178:179], v[246:247], 0, s[28:29]
	s_mov_b32 m0, s47
	ds_read_b128 v[198:201], v176
	ds_read_b128 v[202:205], v176 offset:1024
	ds_read_b128 v[206:209], v176 offset:2048
	ds_read_b128 v[210:213], v176 offset:3072
	ds_read_b128 v[214:217], v176 offset:4096
	ds_read_b128 v[218:221], v176 offset:5120
	ds_read_b128 v[222:225], v176 offset:6144
	ds_read_b128 v[226:229], v176 offset:7168
	global_load_lds_dwordx4 v[178:179], off
	v_add_u32_e32 v178, 0xe000, v148
	v_lshl_add_u64 v[248:249], v[134:135], 0, s[44:45]
	v_readfirstlane_b32 s47, v178
	v_lshl_add_u64 v[230:231], v[248:249], 0, s[28:29]
	s_mov_b32 m0, s47
	s_nop 0
	global_load_lds_dwordx4 v[230:231], off
	s_waitcnt lgkmcnt(8)
	s_barrier
	s_waitcnt lgkmcnt(0)
	v_mfma_f32_16x16x32_f16 v[126:129], v[198:201], v[182:185], v[126:129]
	v_mfma_f32_16x16x32_f16 v[122:125], v[198:201], v[190:193], v[122:125]
	v_mfma_f32_16x16x32_f16 v[118:121], v[206:209], v[182:185], v[118:121]
	v_mfma_f32_16x16x32_f16 v[114:117], v[206:209], v[190:193], v[114:117]
	v_mfma_f32_16x16x32_f16 v[110:113], v[214:217], v[182:185], v[110:113]
	v_mfma_f32_16x16x32_f16 v[106:109], v[214:217], v[190:193], v[106:109]
	v_mfma_f32_16x16x32_f16 v[102:105], v[222:225], v[182:185], v[102:105]
	v_mfma_f32_16x16x32_f16 v[98:101], v[222:225], v[190:193], v[98:101]
	v_mfma_f32_16x16x32_f16 v[126:129], v[202:205], v[186:189], v[126:129]
	v_mfma_f32_16x16x32_f16 v[122:125], v[202:205], v[194:197], v[122:125]
	v_mfma_f32_16x16x32_f16 v[118:121], v[210:213], v[186:189], v[118:121]
	v_mfma_f32_16x16x32_f16 v[114:117], v[210:213], v[194:197], v[114:117]
	v_mfma_f32_16x16x32_f16 v[110:113], v[218:221], v[186:189], v[110:113]
	v_mfma_f32_16x16x32_f16 v[106:109], v[218:221], v[194:197], v[106:109]
	v_mfma_f32_16x16x32_f16 v[102:105], v[226:229], v[186:189], v[102:105]
	v_mfma_f32_16x16x32_f16 v[98:101], v[226:229], v[194:197], v[98:101]
	s_barrier
	v_lshl_add_u64 v[250:251], v[140:141], 0, s[44:45]
	v_readfirstlane_b32 s47, v142
	v_lshl_add_u64 v[252:253], v[250:251], 0, s[30:31]
	s_mov_b32 m0, s47
	ds_read_b128 v[230:233], v162
	ds_read_b128 v[234:237], v163
	ds_read_b128 v[238:241], v164
	ds_read_b128 v[242:245], v165
	global_load_lds_dwordx4 v[252:253], off
	v_lshl_add_u64 v[252:253], v[138:139], 0, s[44:45]
	v_readfirstlane_b32 s47, v143
	v_lshl_add_u64 v[254:255], v[252:253], 0, s[30:31]
	s_mov_b32 m0, s47
	s_nop 0
	global_load_lds_dwordx4 v[254:255], off
	s_barrier
	s_waitcnt lgkmcnt(0)
	v_mfma_f32_16x16x32_f16 v[94:97], v[198:201], v[230:233], v[94:97]
	v_mfma_f32_16x16x32_f16 v[90:93], v[198:201], v[238:241], v[90:93]
	v_mfma_f32_16x16x32_f16 v[86:89], v[206:209], v[230:233], v[86:89]
	v_mfma_f32_16x16x32_f16 v[82:85], v[206:209], v[238:241], v[82:85]
	v_mfma_f32_16x16x32_f16 v[78:81], v[214:217], v[230:233], v[78:81]
	v_mfma_f32_16x16x32_f16 v[74:77], v[214:217], v[238:241], v[74:77]
	v_mfma_f32_16x16x32_f16 v[70:73], v[222:225], v[230:233], v[70:73]
	v_mfma_f32_16x16x32_f16 v[66:69], v[222:225], v[238:241], v[66:69]
	v_mfma_f32_16x16x32_f16 v[94:97], v[202:205], v[234:237], v[94:97]
	v_mfma_f32_16x16x32_f16 v[90:93], v[202:205], v[242:245], v[90:93]
	v_mfma_f32_16x16x32_f16 v[86:89], v[210:213], v[234:237], v[86:89]
	v_mfma_f32_16x16x32_f16 v[82:85], v[210:213], v[242:245], v[82:85]
	v_mfma_f32_16x16x32_f16 v[78:81], v[218:221], v[234:237], v[78:81]
	v_mfma_f32_16x16x32_f16 v[74:77], v[218:221], v[242:245], v[74:77]
	v_mfma_f32_16x16x32_f16 v[70:73], v[226:229], v[234:237], v[70:73]
	v_mfma_f32_16x16x32_f16 v[66:69], v[226:229], v[242:245], v[66:69]
	v_readfirstlane_b32 s47, v148
	v_lshl_add_u64 v[254:255], v[246:247], 0, s[30:31]
	s_mov_b32 m0, s47
	v_readfirstlane_b32 s47, v149
	s_barrier
	ds_read_b128 v[198:201], v176 offset:16384
	ds_read_b128 v[202:205], v176 offset:17408
	ds_read_b128 v[206:209], v176 offset:18432
	ds_read_b128 v[210:213], v176 offset:19456
	ds_read_b128 v[214:217], v176 offset:20480
	ds_read_b128 v[218:221], v176 offset:21504
	ds_read_b128 v[222:225], v176 offset:22528
	ds_read_b128 v[226:229], v176 offset:23552
	global_load_lds_dwordx4 v[254:255], off
	v_lshl_add_u64 v[254:255], v[248:249], 0, s[30:31]
	s_mov_b32 m0, s47
	s_nop 0
	global_load_lds_dwordx4 v[254:255], off
	s_barrier
	s_waitcnt lgkmcnt(0)
	v_mfma_f32_16x16x32_f16 v[62:65], v[198:201], v[182:185], v[62:65]
	v_mfma_f32_16x16x32_f16 v[58:61], v[198:201], v[190:193], v[58:61]
	v_mfma_f32_16x16x32_f16 v[54:57], v[206:209], v[182:185], v[54:57]
	v_mfma_f32_16x16x32_f16 v[50:53], v[206:209], v[190:193], v[50:53]
	v_mfma_f32_16x16x32_f16 v[46:49], v[214:217], v[182:185], v[46:49]
	v_mfma_f32_16x16x32_f16 v[42:45], v[214:217], v[190:193], v[42:45]
	v_mfma_f32_16x16x32_f16 v[38:41], v[222:225], v[182:185], v[38:41]
	v_mfma_f32_16x16x32_f16 v[34:37], v[222:225], v[190:193], v[34:37]
	v_mfma_f32_16x16x32_f16 v[62:65], v[202:205], v[186:189], v[62:65]
	v_mfma_f32_16x16x32_f16 v[58:61], v[202:205], v[194:197], v[58:61]
	v_mfma_f32_16x16x32_f16 v[54:57], v[210:213], v[186:189], v[54:57]
	v_mfma_f32_16x16x32_f16 v[50:53], v[210:213], v[194:197], v[50:53]
	v_mfma_f32_16x16x32_f16 v[46:49], v[218:221], v[186:189], v[46:49]
	v_mfma_f32_16x16x32_f16 v[42:45], v[218:221], v[194:197], v[42:45]
	v_mfma_f32_16x16x32_f16 v[38:41], v[226:229], v[186:189], v[38:41]
	v_mfma_f32_16x16x32_f16 v[34:37], v[226:229], v[194:197], v[34:37]
	s_barrier
	v_readfirstlane_b32 s47, v154
	v_lshl_add_u64 v[182:183], v[250:251], 0, s[34:35]
	s_mov_b32 m0, s47
	v_readfirstlane_b32 s47, v155
	global_load_lds_dwordx4 v[182:183], off
	v_lshl_add_u64 v[182:183], v[252:253], 0, s[34:35]
	s_mov_b32 m0, s47
	s_nop 0
	global_load_lds_dwordx4 v[182:183], off
	s_waitcnt vmcnt(6)
	s_barrier
	v_mfma_f32_16x16x32_f16 v[30:33], v[198:201], v[230:233], v[30:33]
	v_mfma_f32_16x16x32_f16 v[26:29], v[198:201], v[238:241], v[26:29]
	v_mfma_f32_16x16x32_f16 v[22:25], v[206:209], v[230:233], v[22:25]
	v_mfma_f32_16x16x32_f16 v[18:21], v[206:209], v[238:241], v[18:21]
	v_mfma_f32_16x16x32_f16 v[14:17], v[214:217], v[230:233], v[14:17]
	v_mfma_f32_16x16x32_f16 v[10:13], v[214:217], v[238:241], v[10:13]
	v_mfma_f32_16x16x32_f16 v[6:9], v[222:225], v[230:233], v[6:9]
	v_mfma_f32_16x16x32_f16 v[2:5], v[222:225], v[238:241], v[2:5]
	v_mfma_f32_16x16x32_f16 v[30:33], v[202:205], v[234:237], v[30:33]
	v_mfma_f32_16x16x32_f16 v[26:29], v[202:205], v[242:245], v[26:29]
	v_mfma_f32_16x16x32_f16 v[22:25], v[210:213], v[234:237], v[22:25]
	v_mfma_f32_16x16x32_f16 v[18:21], v[210:213], v[242:245], v[18:21]
	v_mfma_f32_16x16x32_f16 v[14:17], v[218:221], v[234:237], v[14:17]
	v_mfma_f32_16x16x32_f16 v[10:13], v[218:221], v[242:245], v[10:13]
	v_mfma_f32_16x16x32_f16 v[6:9], v[226:229], v[234:237], v[6:9]
	v_mfma_f32_16x16x32_f16 v[2:5], v[226:229], v[242:245], v[2:5]
	s_barrier
	ds_read_b128 v[182:185], v144
	ds_read_b128 v[186:189], v145
	ds_read_b128 v[190:193], v146
	ds_read_b128 v[194:197], v147
	v_readfirstlane_b32 s47, v156
	v_lshl_add_u64 v[230:231], v[246:247], 0, s[34:35]
	s_mov_b32 m0, s47
	v_readfirstlane_b32 s47, v157
	ds_read_b128 v[198:201], v176 offset:32768
	ds_read_b128 v[202:205], v176 offset:33792
	ds_read_b128 v[206:209], v176 offset:34816
	ds_read_b128 v[210:213], v176 offset:35840
	ds_read_b128 v[214:217], v176 offset:36864
	ds_read_b128 v[218:221], v176 offset:37888
	ds_read_b128 v[222:225], v176 offset:38912
	ds_read_b128 v[226:229], v176 offset:39936
	global_load_lds_dwordx4 v[230:231], off
	v_lshl_add_u64 v[230:231], v[248:249], 0, s[34:35]
	s_mov_b32 m0, s47
	s_nop 0
	global_load_lds_dwordx4 v[230:231], off
	s_waitcnt lgkmcnt(8)
	s_barrier
	s_waitcnt lgkmcnt(0)
	v_mfma_f32_16x16x32_f16 v[126:129], v[198:201], v[182:185], v[126:129]
	v_mfma_f32_16x16x32_f16 v[122:125], v[198:201], v[190:193], v[122:125]
	v_mfma_f32_16x16x32_f16 v[118:121], v[206:209], v[182:185], v[118:121]
	v_mfma_f32_16x16x32_f16 v[114:117], v[206:209], v[190:193], v[114:117]
	v_mfma_f32_16x16x32_f16 v[110:113], v[214:217], v[182:185], v[110:113]
	v_mfma_f32_16x16x32_f16 v[106:109], v[214:217], v[190:193], v[106:109]
	v_mfma_f32_16x16x32_f16 v[102:105], v[222:225], v[182:185], v[102:105]
	v_mfma_f32_16x16x32_f16 v[98:101], v[222:225], v[190:193], v[98:101]
	v_mfma_f32_16x16x32_f16 v[126:129], v[202:205], v[186:189], v[126:129]
	v_mfma_f32_16x16x32_f16 v[122:125], v[202:205], v[194:197], v[122:125]
	v_mfma_f32_16x16x32_f16 v[118:121], v[210:213], v[186:189], v[118:121]
	v_mfma_f32_16x16x32_f16 v[114:117], v[210:213], v[194:197], v[114:117]
	v_mfma_f32_16x16x32_f16 v[110:113], v[218:221], v[186:189], v[110:113]
	v_mfma_f32_16x16x32_f16 v[106:109], v[218:221], v[194:197], v[106:109]
	v_mfma_f32_16x16x32_f16 v[102:105], v[226:229], v[186:189], v[102:105]
	v_mfma_f32_16x16x32_f16 v[98:101], v[226:229], v[194:197], v[98:101]
	s_barrier
	v_readfirstlane_b32 s47, v158
	v_lshl_add_u64 v[254:255], v[250:251], 0, s[36:37]
	s_mov_b32 m0, s47
	v_readfirstlane_b32 s47, v160
	ds_read_b128 v[230:233], v150
	ds_read_b128 v[234:237], v151
	ds_read_b128 v[238:241], v152
	ds_read_b128 v[242:245], v153
	global_load_lds_dwordx4 v[254:255], off
	v_lshl_add_u64 v[254:255], v[252:253], 0, s[36:37]
	s_mov_b32 m0, s47
	s_nop 0
	global_load_lds_dwordx4 v[254:255], off
	s_barrier
	s_waitcnt lgkmcnt(0)
	v_mfma_f32_16x16x32_f16 v[94:97], v[198:201], v[230:233], v[94:97]
	v_mfma_f32_16x16x32_f16 v[90:93], v[198:201], v[238:241], v[90:93]
	v_mfma_f32_16x16x32_f16 v[86:89], v[206:209], v[230:233], v[86:89]
	v_mfma_f32_16x16x32_f16 v[82:85], v[206:209], v[238:241], v[82:85]
	v_mfma_f32_16x16x32_f16 v[78:81], v[214:217], v[230:233], v[78:81]
	v_mfma_f32_16x16x32_f16 v[74:77], v[214:217], v[238:241], v[74:77]
	v_mfma_f32_16x16x32_f16 v[70:73], v[222:225], v[230:233], v[70:73]
	v_mfma_f32_16x16x32_f16 v[66:69], v[222:225], v[238:241], v[66:69]
	v_mfma_f32_16x16x32_f16 v[94:97], v[202:205], v[234:237], v[94:97]
	v_mfma_f32_16x16x32_f16 v[90:93], v[202:205], v[242:245], v[90:93]
	v_mfma_f32_16x16x32_f16 v[86:89], v[210:213], v[234:237], v[86:89]
	v_mfma_f32_16x16x32_f16 v[82:85], v[210:213], v[242:245], v[82:85]
	v_mfma_f32_16x16x32_f16 v[78:81], v[218:221], v[234:237], v[78:81]
	v_mfma_f32_16x16x32_f16 v[74:77], v[218:221], v[242:245], v[74:77]
	v_mfma_f32_16x16x32_f16 v[70:73], v[226:229], v[234:237], v[70:73]
	v_mfma_f32_16x16x32_f16 v[66:69], v[226:229], v[242:245], v[66:69]
	v_readfirstlane_b32 s47, v161
	v_lshl_add_u64 v[246:247], v[246:247], 0, s[36:37]
	s_mov_b32 m0, s47
	v_readfirstlane_b32 s47, v166
	s_barrier
	ds_read_b128 v[198:201], v176 offset:49152
	ds_read_b128 v[202:205], v176 offset:50176
	ds_read_b128 v[206:209], v176 offset:51200
	ds_read_b128 v[210:213], v176 offset:52224
	ds_read_b128 v[214:217], v176 offset:53248
	ds_read_b128 v[218:221], v176 offset:54272
	ds_read_b128 v[222:225], v176 offset:55296
	ds_read_b128 v[226:229], v176 offset:56320
	global_load_lds_dwordx4 v[246:247], off
	v_lshl_add_u64 v[246:247], v[248:249], 0, s[36:37]
	s_mov_b32 m0, s47
	s_nop 0
	global_load_lds_dwordx4 v[246:247], off
	s_barrier
	s_waitcnt lgkmcnt(0)
	v_mfma_f32_16x16x32_f16 v[62:65], v[198:201], v[182:185], v[62:65]
	v_mfma_f32_16x16x32_f16 v[58:61], v[198:201], v[190:193], v[58:61]
	v_mfma_f32_16x16x32_f16 v[54:57], v[206:209], v[182:185], v[54:57]
	v_mfma_f32_16x16x32_f16 v[50:53], v[206:209], v[190:193], v[50:53]
	v_mfma_f32_16x16x32_f16 v[46:49], v[214:217], v[182:185], v[46:49]
	v_mfma_f32_16x16x32_f16 v[42:45], v[214:217], v[190:193], v[42:45]
	v_mfma_f32_16x16x32_f16 v[38:41], v[222:225], v[182:185], v[38:41]
	v_mfma_f32_16x16x32_f16 v[34:37], v[222:225], v[190:193], v[34:37]
	v_mfma_f32_16x16x32_f16 v[62:65], v[202:205], v[186:189], v[62:65]
	v_mfma_f32_16x16x32_f16 v[58:61], v[202:205], v[194:197], v[58:61]
	v_mfma_f32_16x16x32_f16 v[54:57], v[210:213], v[186:189], v[54:57]
	v_mfma_f32_16x16x32_f16 v[50:53], v[210:213], v[194:197], v[50:53]
	v_mfma_f32_16x16x32_f16 v[46:49], v[218:221], v[186:189], v[46:49]
	v_mfma_f32_16x16x32_f16 v[42:45], v[218:221], v[194:197], v[42:45]
	v_mfma_f32_16x16x32_f16 v[38:41], v[226:229], v[186:189], v[38:41]
	v_mfma_f32_16x16x32_f16 v[34:37], v[226:229], v[194:197], v[34:37]
	s_barrier
	v_readfirstlane_b32 s47, v168
	v_lshl_add_u64 v[182:183], v[250:251], 0, s[38:39]
	s_mov_b32 m0, s47
	v_readfirstlane_b32 s47, v169
	global_load_lds_dwordx4 v[182:183], off
	v_lshl_add_u64 v[182:183], v[252:253], 0, s[38:39]
	s_mov_b32 m0, s47
	s_nop 0
	global_load_lds_dwordx4 v[182:183], off
	s_waitcnt vmcnt(6)
	s_barrier
	v_mfma_f32_16x16x32_f16 v[30:33], v[198:201], v[230:233], v[30:33]
	v_mfma_f32_16x16x32_f16 v[26:29], v[198:201], v[238:241], v[26:29]
	v_mfma_f32_16x16x32_f16 v[22:25], v[206:209], v[230:233], v[22:25]
	v_mfma_f32_16x16x32_f16 v[18:21], v[206:209], v[238:241], v[18:21]
	v_mfma_f32_16x16x32_f16 v[14:17], v[214:217], v[230:233], v[14:17]
	v_mfma_f32_16x16x32_f16 v[10:13], v[214:217], v[238:241], v[10:13]
	v_mfma_f32_16x16x32_f16 v[6:9], v[222:225], v[230:233], v[6:9]
	v_mfma_f32_16x16x32_f16 v[2:5], v[222:225], v[238:241], v[2:5]
	v_mfma_f32_16x16x32_f16 v[30:33], v[202:205], v[234:237], v[30:33]
	v_mfma_f32_16x16x32_f16 v[26:29], v[202:205], v[242:245], v[26:29]
	v_mfma_f32_16x16x32_f16 v[22:25], v[210:213], v[234:237], v[22:25]
	v_mfma_f32_16x16x32_f16 v[18:21], v[210:213], v[242:245], v[18:21]
	v_mfma_f32_16x16x32_f16 v[14:17], v[218:221], v[234:237], v[14:17]
	v_mfma_f32_16x16x32_f16 v[10:13], v[218:221], v[242:245], v[10:13]
	v_mfma_f32_16x16x32_f16 v[6:9], v[226:229], v[234:237], v[6:9]
	v_mfma_f32_16x16x32_f16 v[2:5], v[226:229], v[242:245], v[2:5]
	s_add_i32 s46, s46, 2
	s_add_u32 s44, s44, 0x100
	s_addc_u32 s45, s45, 0
	s_cmp_lt_u32 s46, 28
	s_barrier
	s_cbranch_scc1 .LBB10_12
	s_add_u32 s42, s42, 0x80f80
	s_addc_u32 s43, s43, 0
	v_readfirstlane_b32 s44, v177
	v_lshl_add_u64 v[130:131], v[130:131], 1, s[42:43]
	s_mov_b32 m0, s44
	ds_read_b128 v[134:137], v171
	ds_read_b128 v[138:141], v173
	ds_read_b128 v[154:157], v174
	ds_read_b128 v[168:171], v175
	ds_read_b128 v[182:185], v176
	ds_read_b128 v[186:189], v176 offset:1024
	ds_read_b128 v[190:193], v176 offset:2048
	ds_read_b128 v[194:197], v176 offset:3072
	ds_read_b128 v[198:201], v176 offset:4096
	ds_read_b128 v[202:205], v176 offset:5120
	ds_read_b128 v[206:209], v176 offset:6144
	ds_read_b128 v[210:213], v176 offset:7168
	global_load_lds_dwordx4 v[130:131], off
	v_lshl_add_u64 v[130:131], v[132:133], 1, s[42:43]
	v_readfirstlane_b32 s42, v178
	s_mov_b32 m0, s42
	s_nop 0
	global_load_lds_dwordx4 v[130:131], off
	s_barrier
	s_waitcnt lgkmcnt(0)
	v_mfma_f32_16x16x32_f16 v[122:125], v[182:185], v[154:157], v[122:125]
	v_mfma_f32_16x16x32_f16 v[110:113], v[198:201], v[134:137], v[110:113]
	v_mfma_f32_16x16x32_f16 v[98:101], v[206:209], v[154:157], v[98:101]
	v_mfma_f32_16x16x32_f16 v[126:129], v[182:185], v[134:137], v[126:129]
	v_mfma_f32_16x16x32_f16 v[122:125], v[186:189], v[168:171], v[122:125]
	v_mfma_f32_16x16x32_f16 v[118:121], v[190:193], v[134:137], v[118:121]
	v_mfma_f32_16x16x32_f16 v[114:117], v[190:193], v[154:157], v[114:117]
	v_mfma_f32_16x16x32_f16 v[130:133], v[202:205], v[138:141], v[110:113]
	v_mfma_f32_16x16x32_f16 v[106:109], v[198:201], v[154:157], v[106:109]
	v_mfma_f32_16x16x32_f16 v[102:105], v[206:209], v[134:137], v[102:105]
	v_mfma_f32_16x16x32_f16 v[98:101], v[210:213], v[168:171], v[98:101]
	v_mfma_f32_16x16x32_f16 v[126:129], v[186:189], v[138:141], v[126:129]
	v_mfma_f32_16x16x32_f16 v[118:121], v[194:197], v[138:141], v[118:121]
	v_mfma_f32_16x16x32_f16 v[114:117], v[194:197], v[168:171], v[114:117]
	v_mfma_f32_16x16x32_f16 v[214:217], v[202:205], v[168:171], v[106:109]
	v_mfma_f32_16x16x32_f16 v[102:105], v[210:213], v[138:141], v[102:105]
	s_barrier
	ds_read_b128 v[106:109], v162
	ds_read_b128 v[110:113], v163
	ds_read_b128 v[160:163], v164
	ds_read_b128 v[218:221], v165
	s_barrier
	s_waitcnt lgkmcnt(0)
	v_mfma_f32_16x16x32_f16 v[82:85], v[190:193], v[160:163], v[82:85]
	v_mfma_f32_16x16x32_f16 v[78:81], v[198:201], v[106:109], v[78:81]
	v_mfma_f32_16x16x32_f16 v[74:77], v[198:201], v[160:163], v[74:77]
	v_mfma_f32_16x16x32_f16 v[70:73], v[206:209], v[106:109], v[70:73]
	v_mfma_f32_16x16x32_f16 v[66:69], v[206:209], v[160:163], v[66:69]
	v_mfma_f32_16x16x32_f16 v[94:97], v[182:185], v[106:109], v[94:97]
	v_mfma_f32_16x16x32_f16 v[90:93], v[182:185], v[160:163], v[90:93]
	v_mfma_f32_16x16x32_f16 v[86:89], v[190:193], v[106:109], v[86:89]
	v_mfma_f32_16x16x32_f16 v[82:85], v[194:197], v[218:221], v[82:85]
	v_mfma_f32_16x16x32_f16 v[78:81], v[202:205], v[110:113], v[78:81]
	v_mfma_f32_16x16x32_f16 v[74:77], v[202:205], v[218:221], v[74:77]
	v_mfma_f32_16x16x32_f16 v[70:73], v[210:213], v[110:113], v[70:73]
	v_mfma_f32_16x16x32_f16 v[66:69], v[210:213], v[218:221], v[66:69]
	v_mfma_f32_16x16x32_f16 v[222:225], v[186:189], v[110:113], v[94:97]
	v_mfma_f32_16x16x32_f16 v[182:185], v[186:189], v[218:221], v[90:93]
	v_mfma_f32_16x16x32_f16 v[86:89], v[194:197], v[110:113], v[86:89]
	s_barrier
	ds_read_b128 v[90:93], v176 offset:16384
	ds_read_b128 v[94:97], v176 offset:17408
	ds_read_b128 v[186:189], v176 offset:18432
	ds_read_b128 v[190:193], v176 offset:19456
	ds_read_b128 v[194:197], v176 offset:20480
	ds_read_b128 v[198:201], v176 offset:21504
	ds_read_b128 v[202:205], v176 offset:22528
	ds_read_b128 v[206:209], v176 offset:23552
	s_waitcnt vmcnt(4)
	s_barrier
	s_waitcnt lgkmcnt(0)
	v_mfma_f32_16x16x32_f16 v[46:49], v[194:197], v[134:137], v[46:49]
	v_mfma_f32_16x16x32_f16 v[42:45], v[194:197], v[154:157], v[42:45]
	v_mfma_f32_16x16x32_f16 v[38:41], v[202:205], v[134:137], v[38:41]
	v_mfma_f32_16x16x32_f16 v[34:37], v[202:205], v[154:157], v[34:37]
	v_mfma_f32_16x16x32_f16 v[62:65], v[90:93], v[134:137], v[62:65]
	v_mfma_f32_16x16x32_f16 v[58:61], v[90:93], v[154:157], v[58:61]
	v_mfma_f32_16x16x32_f16 v[54:57], v[186:189], v[134:137], v[54:57]
	v_mfma_f32_16x16x32_f16 v[50:53], v[186:189], v[154:157], v[50:53]
	v_mfma_f32_16x16x32_f16 v[46:49], v[198:201], v[138:141], v[46:49]
	v_mfma_f32_16x16x32_f16 v[42:45], v[198:201], v[168:171], v[42:45]
	v_mfma_f32_16x16x32_f16 v[38:41], v[206:209], v[138:141], v[38:41]
	v_mfma_f32_16x16x32_f16 v[34:37], v[206:209], v[168:171], v[34:37]
	v_mfma_f32_16x16x32_f16 v[210:213], v[94:97], v[138:141], v[62:65]
	v_mfma_f32_16x16x32_f16 v[226:229], v[94:97], v[168:171], v[58:61]
	v_mfma_f32_16x16x32_f16 v[230:233], v[190:193], v[138:141], v[54:57]
	v_mfma_f32_16x16x32_f16 v[234:237], v[190:193], v[168:171], v[50:53]
	v_mfma_f32_16x16x32_f16 v[2:5], v[202:205], v[160:163], v[2:5]
	v_mfma_f32_16x16x32_f16 v[30:33], v[90:93], v[106:109], v[30:33]
	v_mfma_f32_16x16x32_f16 v[26:29], v[90:93], v[160:163], v[26:29]
	v_mfma_f32_16x16x32_f16 v[22:25], v[186:189], v[106:109], v[22:25]
	v_mfma_f32_16x16x32_f16 v[18:21], v[186:189], v[160:163], v[18:21]
	v_mfma_f32_16x16x32_f16 v[14:17], v[194:197], v[106:109], v[14:17]
	v_mfma_f32_16x16x32_f16 v[10:13], v[194:197], v[160:163], v[10:13]
	v_mfma_f32_16x16x32_f16 v[6:9], v[202:205], v[106:109], v[6:9]
	v_mfma_f32_16x16x32_f16 v[2:5], v[206:209], v[218:221], v[2:5]
	v_mfma_f32_16x16x32_f16 v[138:141], v[94:97], v[110:113], v[30:33]
	v_mfma_f32_16x16x32_f16 v[168:171], v[94:97], v[218:221], v[26:29]
	v_mfma_f32_16x16x32_f16 v[238:241], v[190:193], v[110:113], v[22:25]
	v_mfma_f32_16x16x32_f16 v[186:189], v[190:193], v[218:221], v[18:21]
	v_mfma_f32_16x16x32_f16 v[190:193], v[198:201], v[110:113], v[14:17]
	v_mfma_f32_16x16x32_f16 v[194:197], v[198:201], v[218:221], v[10:13]
	v_mfma_f32_16x16x32_f16 v[198:201], v[206:209], v[110:113], v[6:9]
	s_barrier
	s_nop 0
	ds_read_b128 v[6:9], v144
	ds_read_b128 v[10:13], v145
	ds_read_b128 v[14:17], v146
	ds_read_b128 v[160:163], v147
	ds_read_b128 v[18:21], v176 offset:32768
	ds_read_b128 v[22:25], v176 offset:33792
	ds_read_b128 v[26:29], v176 offset:34816
	ds_read_b128 v[50:53], v176 offset:35840
	ds_read_b128 v[202:205], v176 offset:36864
	ds_read_b128 v[206:209], v176 offset:37888
	ds_read_b128 v[218:221], v176 offset:38912
	ds_read_b128 v[242:245], v176 offset:39936
	s_waitcnt vmcnt(2)
	s_barrier
	s_waitcnt lgkmcnt(0)
	v_mfma_f32_16x16x32_f16 v[30:33], v[18:21], v[6:9], v[126:129]
	v_mfma_f32_16x16x32_f16 v[154:157], v[22:25], v[10:13], v[30:33]
	v_mfma_f32_16x16x32_f16 v[30:33], v[18:21], v[14:17], v[122:125]
	v_mfma_f32_16x16x32_f16 v[110:113], v[22:25], v[160:163], v[30:33]
	v_mfma_f32_16x16x32_f16 v[30:33], v[26:29], v[6:9], v[118:121]
	v_mfma_f32_16x16x32_f16 v[146:149], v[50:53], v[10:13], v[30:33]
	v_mfma_f32_16x16x32_f16 v[30:33], v[26:29], v[14:17], v[114:117]
	v_mfma_f32_16x16x32_f16 v[106:109], v[50:53], v[160:163], v[30:33]
	v_mfma_f32_16x16x32_f16 v[30:33], v[202:205], v[6:9], v[130:133]
	v_mfma_f32_16x16x32_f16 v[142:145], v[206:209], v[10:13], v[30:33]
	v_mfma_f32_16x16x32_f16 v[30:33], v[202:205], v[14:17], v[214:217]
	v_mfma_f32_16x16x32_f16 v[94:97], v[206:209], v[160:163], v[30:33]
	v_mfma_f32_16x16x32_f16 v[30:33], v[218:221], v[6:9], v[102:105]
	v_mfma_f32_16x16x32_f16 v[134:137], v[242:245], v[10:13], v[30:33]
	v_mfma_f32_16x16x32_f16 v[30:33], v[218:221], v[14:17], v[98:101]
	v_mfma_f32_16x16x32_f16 v[90:93], v[242:245], v[160:163], v[30:33]
	s_barrier
	ds_read_b128 v[102:105], v150
	ds_read_b128 v[114:117], v151
	ds_read_b128 v[118:121], v152
	ds_read_b128 v[126:129], v153
	s_waitcnt vmcnt(0)
	s_barrier
	s_waitcnt lgkmcnt(0)
	v_mfma_f32_16x16x32_f16 v[30:33], v[18:21], v[102:105], v[222:225]
	v_mfma_f32_16x16x32_f16 v[18:21], v[18:21], v[118:121], v[182:185]
	v_mfma_f32_16x16x32_f16 v[62:65], v[22:25], v[114:117], v[30:33]
	v_mfma_f32_16x16x32_f16 v[30:33], v[22:25], v[126:129], v[18:21]
	v_mfma_f32_16x16x32_f16 v[18:21], v[26:29], v[102:105], v[86:89]
	v_mfma_f32_16x16x32_f16 v[58:61], v[50:53], v[114:117], v[18:21]
	v_mfma_f32_16x16x32_f16 v[18:21], v[26:29], v[118:121], v[82:85]
	v_mfma_f32_16x16x32_f16 v[26:29], v[50:53], v[126:129], v[18:21]
	v_mfma_f32_16x16x32_f16 v[18:21], v[202:205], v[102:105], v[78:81]
	v_mfma_f32_16x16x32_f16 v[54:57], v[206:209], v[114:117], v[18:21]
	v_mfma_f32_16x16x32_f16 v[18:21], v[202:205], v[118:121], v[74:77]
	v_mfma_f32_16x16x32_f16 v[22:25], v[206:209], v[126:129], v[18:21]
	v_mfma_f32_16x16x32_f16 v[18:21], v[218:221], v[102:105], v[70:73]
	v_mfma_f32_16x16x32_f16 v[50:53], v[242:245], v[114:117], v[18:21]
	v_mfma_f32_16x16x32_f16 v[18:21], v[218:221], v[118:121], v[66:69]
	v_mfma_f32_16x16x32_f16 v[18:21], v[242:245], v[126:129], v[18:21]
	s_barrier
	ds_read_b128 v[86:89], v176 offset:49152
	ds_read_b128 v[150:153], v176 offset:50176
	ds_read_b128 v[182:185], v176 offset:51200
	ds_read_b128 v[202:205], v176 offset:52224
	ds_read_b128 v[206:209], v176 offset:53248
	ds_read_b128 v[214:217], v176 offset:54272
	ds_read_b128 v[218:221], v176 offset:55296
	ds_read_b128 v[174:177], v176 offset:56320
	s_barrier
	s_waitcnt lgkmcnt(0)
	v_mfma_f32_16x16x32_f16 v[66:69], v[86:89], v[6:9], v[210:213]
	v_mfma_f32_16x16x32_f16 v[130:133], v[150:153], v[10:13], v[66:69]
	v_mfma_f32_16x16x32_f16 v[66:69], v[86:89], v[14:17], v[226:229]
	v_mfma_f32_16x16x32_f16 v[78:81], v[150:153], v[160:163], v[66:69]
	v_mfma_f32_16x16x32_f16 v[66:69], v[182:185], v[6:9], v[230:233]
	v_mfma_f32_16x16x32_f16 v[46:49], v[206:209], v[6:9], v[46:49]
	v_mfma_f32_16x16x32_f16 v[6:9], v[218:221], v[6:9], v[38:41]
	v_mfma_f32_16x16x32_f16 v[122:125], v[202:205], v[10:13], v[66:69]
	v_mfma_f32_16x16x32_f16 v[66:69], v[182:185], v[14:17], v[234:237]
	v_mfma_f32_16x16x32_f16 v[42:45], v[206:209], v[14:17], v[42:45]
	v_mfma_f32_16x16x32_f16 v[82:85], v[174:177], v[10:13], v[6:9]
	v_mfma_f32_16x16x32_f16 v[6:9], v[218:221], v[14:17], v[34:37]
	v_mfma_f32_16x16x32_f16 v[74:77], v[202:205], v[160:163], v[66:69]
	v_mfma_f32_16x16x32_f16 v[98:101], v[214:217], v[10:13], v[46:49]
	v_mfma_f32_16x16x32_f16 v[70:73], v[214:217], v[160:163], v[42:45]
	v_mfma_f32_16x16x32_f16 v[66:69], v[174:177], v[160:163], v[6:9]
	v_mfma_f32_16x16x32_f16 v[6:9], v[86:89], v[102:105], v[138:141]
	v_mfma_f32_16x16x32_f16 v[46:49], v[150:153], v[114:117], v[6:9]
	v_mfma_f32_16x16x32_f16 v[6:9], v[86:89], v[118:121], v[168:171]
	v_mfma_f32_16x16x32_f16 v[14:17], v[150:153], v[126:129], v[6:9]
	v_mfma_f32_16x16x32_f16 v[6:9], v[182:185], v[102:105], v[238:241]
	v_mfma_f32_16x16x32_f16 v[42:45], v[202:205], v[114:117], v[6:9]
	v_mfma_f32_16x16x32_f16 v[6:9], v[182:185], v[118:121], v[186:189]
	v_mfma_f32_16x16x32_f16 v[10:13], v[202:205], v[126:129], v[6:9]
	v_mfma_f32_16x16x32_f16 v[6:9], v[206:209], v[102:105], v[190:193]
	v_mfma_f32_16x16x32_f16 v[38:41], v[214:217], v[114:117], v[6:9]
	v_mfma_f32_16x16x32_f16 v[6:9], v[206:209], v[118:121], v[194:197]
	v_mfma_f32_16x16x32_f16 v[34:37], v[218:221], v[102:105], v[198:201]
	v_mfma_f32_16x16x32_f16 v[2:5], v[218:221], v[118:121], v[2:5]
	v_mfma_f32_16x16x32_f16 v[6:9], v[214:217], v[126:129], v[6:9]
	v_mfma_f32_16x16x32_f16 v[34:37], v[174:177], v[114:117], v[34:37]
	v_mfma_f32_16x16x32_f16 v[2:5], v[174:177], v[126:129], v[2:5]
	s_cmpk_gt_u32 s61, 0xff
	s_barrier
	s_cbranch_scc1 .LBB10_15
	s_barrier
